# GEMM unit transitions (NSA_OUT FFN_GU FFN_DN FOX_OUT MOE_GU MOE_DN): first two super-phase vmcnt waits of a unit relaxed by the epilogue's fixed VMEM count so epilogue stores/row-scale loads drain und
# speedup vs baseline: 1.0002x; 1.0002x over previous
.LBB0_1328:
	s_mov_b32 s100, 0
	v_readlane_b32 s2, v254, 16
	s_cmp_lt_i32 s2, 8
	v_readlane_b32 s3, v254, 17
	s_cselect_b64 s[4:5], -1, 0
	s_add_u32 s2, s86, 0x4c800000
	s_addc_u32 s3, s87, 0
	s_and_b64 s[0:1], s[4:5], s[0:1]
	s_andn2_b64 vcc, exec, s[0:1]
	s_cbranch_vccnz .LBB0_1353
	v_readlane_b32 s4, v254, 14
	s_cmpk_gt_i32 s4, 0x3ff
	v_readfirstlane_b32 s9, v0
	s_cbranch_scc1 .LBB0_1353
	v_readlane_b32 s5, v254, 14
	s_ashr_i32 s33, s5, 31
	s_lshr_b32 s4, s33, 29
	s_add_i32 s7, s5, s4
	s_and_b32 s4, s7, -8
	s_sub_i32 s8, s5, s4
	s_cmp_gt_i32 s8, -1
	s_cbranch_scc0 .LBB0_1332
	s_lshl_b32 s6, s8, 7
	s_cbranch_execz .LBB0_1333
	s_branch .LBB0_1334

.LBB0_1345:
	s_ashr_i32 s23, s22, 31
	s_lshl_b64 s[24:25], s[22:23], 20
	v_readlane_b32 s26, v254, 22
	v_readlane_b32 s27, v254, 23
	s_add_u32 s24, s26, s24
	s_addc_u32 s25, s27, s25
	s_and_b64 s[26:27], s[8:9], exec
	s_cselect_b32 s23, s25, s31
	s_cselect_b32 s55, s24, s30
	s_ashr_i32 s21, s20, 31
	s_lshl_b64 s[26:27], s[20:21], 20
	s_add_u32 s26, s38, s26
	s_addc_u32 s27, s39, s27
	s_and_b64 s[36:37], s[8:9], exec
	s_cselect_b32 s21, s27, s35
	s_cselect_b32 s56, s26, s34
	s_add_u32 s30, s30, 0x80080
	s_addc_u32 s31, s31, 0
	s_add_u32 s57, s34, 0x100
	s_addc_u32 s58, s35, 0
	s_mov_b32 s59, -2
	ds_read_b128 v[154:157], v150
	ds_read_b128 v[158:161], v150 offset:1024
	ds_read_b128 v[162:165], v150 offset:2048
	ds_read_b128 v[166:169], v150 offset:3072
	ds_read_b128 v[170:173], v151
	ds_read_b128 v[174:177], v151 offset:1024
	ds_read_b128 v[178:181], v151 offset:2048
	ds_read_b128 v[182:185], v151 offset:3072
	s_add_u32 s34, s30, 0xfff80080
	s_addc_u32 s35, s31, -1
	s_cmp_eq_u32 s59, 28
	s_cselect_b32 s37, s23, s35
	s_cselect_b32 s36, s55, s34
	s_cselect_b32 s35, s21, s58
	s_cselect_b32 s34, s56, s57
	v_lshl_add_u64 v[146:147], s[30:31], 0, v[138:139]
	s_add_i32 m0, s29, 0xc000
	ds_read_b128 v[186:189], v152
	ds_read_b128 v[190:193], v152 offset:1024
	ds_read_b128 v[194:197], v152 offset:2048
	ds_read_b128 v[198:201], v152 offset:3072
	ds_read_b128 v[202:205], v152 offset:4096
	ds_read_b128 v[206:209], v152 offset:5120
	ds_read_b128 v[210:213], v152 offset:6144
	ds_read_b128 v[214:217], v152 offset:7168
	global_load_lds_dwordx4 v[146:147], off
	v_lshl_add_u64 v[146:147], s[30:31], 0, v[140:141]
	s_add_i32 m0, s29, 0xe000
	s_nop 0
	global_load_lds_dwordx4 v[146:147], off
	s_cmp_lg_u32 s100, 0
	s_cbranch_scc1 .Lrx_1346_0
	s_waitcnt vmcnt(8)
.Lrx_1346_0:
	s_waitcnt vmcnt(24)
	s_waitcnt lgkmcnt(0)
	s_setprio 1
	s_barrier
	v_mfma_f32_16x16x32_bf16 v[126:129], v[154:157], v[186:189], 0
	v_mfma_f32_16x16x32_bf16 v[122:125], v[162:165], v[186:189], 0
	v_mfma_f32_16x16x32_bf16 v[118:121], v[154:157], v[194:197], 0
	v_mfma_f32_16x16x32_bf16 v[110:113], v[162:165], v[194:197], 0
	v_mfma_f32_16x16x32_bf16 v[102:105], v[154:157], v[202:205], 0
	v_mfma_f32_16x16x32_bf16 v[94:97], v[162:165], v[202:205], 0
	v_mfma_f32_16x16x32_bf16 v[86:89], v[154:157], v[210:213], 0
	v_mfma_f32_16x16x32_bf16 v[78:81], v[162:165], v[210:213], 0
	v_mfma_f32_16x16x32_bf16 v[126:129], v[158:161], v[190:193], v[126:129]
	v_mfma_f32_16x16x32_bf16 v[122:125], v[166:169], v[190:193], v[122:125]
	v_mfma_f32_16x16x32_bf16 v[118:121], v[158:161], v[198:201], v[118:121]
	v_mfma_f32_16x16x32_bf16 v[110:113], v[166:169], v[198:201], v[110:113]
	v_mfma_f32_16x16x32_bf16 v[102:105], v[158:161], v[206:209], v[102:105]
	v_mfma_f32_16x16x32_bf16 v[94:97], v[166:169], v[206:209], v[94:97]
	v_mfma_f32_16x16x32_bf16 v[86:89], v[158:161], v[214:217], v[86:89]
	v_mfma_f32_16x16x32_bf16 v[78:81], v[166:169], v[214:217], v[78:81]
	s_setprio 0
	s_setprio 1
	v_mfma_f32_16x16x32_bf16 v[114:117], v[170:173], v[186:189], 0
	v_mfma_f32_16x16x32_bf16 v[106:109], v[178:181], v[186:189], 0
	v_mfma_f32_16x16x32_bf16 v[98:101], v[170:173], v[194:197], 0
	v_mfma_f32_16x16x32_bf16 v[90:93], v[178:181], v[194:197], 0
	v_mfma_f32_16x16x32_bf16 v[82:85], v[170:173], v[202:205], 0
	v_mfma_f32_16x16x32_bf16 v[74:77], v[178:181], v[202:205], 0
	v_mfma_f32_16x16x32_bf16 v[70:73], v[170:173], v[210:213], 0
	v_mfma_f32_16x16x32_bf16 v[66:69], v[178:181], v[210:213], 0
	v_mfma_f32_16x16x32_bf16 v[114:117], v[174:177], v[190:193], v[114:117]
	v_mfma_f32_16x16x32_bf16 v[106:109], v[182:185], v[190:193], v[106:109]
	v_mfma_f32_16x16x32_bf16 v[98:101], v[174:177], v[198:201], v[98:101]
	v_mfma_f32_16x16x32_bf16 v[90:93], v[182:185], v[198:201], v[90:93]
	v_mfma_f32_16x16x32_bf16 v[82:85], v[174:177], v[206:209], v[82:85]
	v_mfma_f32_16x16x32_bf16 v[74:77], v[182:185], v[206:209], v[74:77]
	v_mfma_f32_16x16x32_bf16 v[70:73], v[174:177], v[214:217], v[70:73]
	v_mfma_f32_16x16x32_bf16 v[66:69], v[182:185], v[214:217], v[66:69]
	s_barrier
	s_setprio 0
	s_add_i32 s60, s48, s40
	v_lshl_add_u64 v[146:147], s[34:35], 0, v[132:133]
	s_mov_b32 m0, s60
	ds_read_b128 v[186:189], v152 offset:16384
	ds_read_b128 v[190:193], v152 offset:17408
	ds_read_b128 v[194:197], v152 offset:18432
	ds_read_b128 v[198:201], v152 offset:19456
	ds_read_b128 v[202:205], v152 offset:20480
	ds_read_b128 v[206:209], v152 offset:21504
	ds_read_b128 v[210:213], v152 offset:22528
	ds_read_b128 v[214:217], v152 offset:23552
	global_load_lds_dwordx4 v[146:147], off
	s_add_i32 m0, s60, 0x2000
	s_add_u32 s60, s34, 0x80000
	v_lshl_add_u64 v[218:219], s[34:35], 0, v[136:137]
	s_addc_u32 s61, s35, 0
	s_add_i32 s62, s49, s40
	global_load_lds_dwordx4 v[218:219], off
	v_lshl_add_u64 v[220:221], s[60:61], 0, v[132:133]
	s_mov_b32 m0, s62
	v_lshl_add_u64 v[222:223], s[36:37], 0, v[134:135]
	global_load_lds_dwordx4 v[220:221], off
	v_lshl_add_u64 v[220:221], s[60:61], 0, v[136:137]
	s_add_i32 m0, s62, 0x2000
	s_nop 0
	global_load_lds_dwordx4 v[220:221], off
	v_lshl_add_u64 v[220:221], s[36:37], 0, v[130:131]
	s_mov_b32 m0, s29
	s_nop 0
	global_load_lds_dwordx4 v[220:221], off
	s_mov_b32 m0, s41
	s_nop 0
	global_load_lds_dwordx4 v[222:223], off
	s_cmp_lg_u32 s100, 0
	s_cbranch_scc1 .Lrx_1346_1
	s_waitcnt vmcnt(8)
.Lrx_1346_1:
	s_waitcnt vmcnt(24)
	s_mov_b32 s100, 1
	s_waitcnt lgkmcnt(0)
	s_setprio 1
	s_barrier
	v_mfma_f32_16x16x32_bf16 v[62:65], v[154:157], v[186:189], 0
	v_mfma_f32_16x16x32_bf16 v[58:61], v[162:165], v[186:189], 0
	v_mfma_f32_16x16x32_bf16 v[54:57], v[154:157], v[194:197], 0
	v_mfma_f32_16x16x32_bf16 v[46:49], v[162:165], v[194:197], 0
	v_mfma_f32_16x16x32_bf16 v[38:41], v[154:157], v[202:205], 0
	v_mfma_f32_16x16x32_bf16 v[30:33], v[162:165], v[202:205], 0
	v_mfma_f32_16x16x32_bf16 v[22:25], v[154:157], v[210:213], 0
	v_mfma_f32_16x16x32_bf16 v[14:17], v[162:165], v[210:213], 0
	v_mfma_f32_16x16x32_bf16 v[62:65], v[158:161], v[190:193], v[62:65]
	v_mfma_f32_16x16x32_bf16 v[58:61], v[166:169], v[190:193], v[58:61]
	v_mfma_f32_16x16x32_bf16 v[54:57], v[158:161], v[198:201], v[54:57]
	v_mfma_f32_16x16x32_bf16 v[46:49], v[166:169], v[198:201], v[46:49]
	v_mfma_f32_16x16x32_bf16 v[38:41], v[158:161], v[206:209], v[38:41]
	v_mfma_f32_16x16x32_bf16 v[30:33], v[166:169], v[206:209], v[30:33]
	v_mfma_f32_16x16x32_bf16 v[22:25], v[158:161], v[214:217], v[22:25]
	v_mfma_f32_16x16x32_bf16 v[14:17], v[166:169], v[214:217], v[14:17]
	s_setprio 0
	s_setprio 1
	v_mfma_f32_16x16x32_bf16 v[50:53], v[170:173], v[186:189], 0
	v_mfma_f32_16x16x32_bf16 v[42:45], v[178:181], v[186:189], 0
	v_mfma_f32_16x16x32_bf16 v[34:37], v[170:173], v[194:197], 0
	v_mfma_f32_16x16x32_bf16 v[26:29], v[178:181], v[194:197], 0
	v_mfma_f32_16x16x32_bf16 v[18:21], v[170:173], v[202:205], 0
	v_mfma_f32_16x16x32_bf16 v[10:13], v[178:181], v[202:205], 0
	v_mfma_f32_16x16x32_bf16 v[6:9], v[170:173], v[210:213], 0
	v_mfma_f32_16x16x32_bf16 v[2:5], v[178:181], v[210:213], 0
	v_mfma_f32_16x16x32_bf16 v[50:53], v[174:177], v[190:193], v[50:53]
	v_mfma_f32_16x16x32_bf16 v[42:45], v[182:185], v[190:193], v[42:45]
	v_mfma_f32_16x16x32_bf16 v[34:37], v[174:177], v[198:201], v[34:37]
	v_mfma_f32_16x16x32_bf16 v[26:29], v[182:185], v[198:201], v[26:29]
	v_mfma_f32_16x16x32_bf16 v[18:21], v[174:177], v[206:209], v[18:21]
	v_mfma_f32_16x16x32_bf16 v[10:13], v[182:185], v[206:209], v[10:13]
	v_mfma_f32_16x16x32_bf16 v[6:9], v[174:177], v[214:217], v[6:9]
	v_mfma_f32_16x16x32_bf16 v[2:5], v[182:185], v[214:217], v[2:5]
	s_barrier
	s_setprio 0
	s_add_i32 s60, 0, 0x18000
	v_add_u32_e32 v153, s60, v148
	s_add_i32 s61, 0, 0x1c000
	ds_read_b128 v[154:157], v153
	ds_read_b128 v[158:161], v153 offset:1024
	ds_read_b128 v[162:165], v153 offset:2048
	ds_read_b128 v[166:169], v153 offset:3072
	v_add_u32_e32 v153, s61, v148
	ds_read_b128 v[170:173], v153
	ds_read_b128 v[174:177], v153 offset:1024
	ds_read_b128 v[178:181], v153 offset:2048
	ds_read_b128 v[182:185], v153 offset:3072
	s_add_u32 s36, s36, 0x80000
	s_addc_u32 s37, s37, 0
	s_mov_b32 m0, s42
	v_lshl_add_u64 v[224:225], s[36:37], 0, v[130:131]
	ds_read_b128 v[186:189], v152 offset:32768
	ds_read_b128 v[190:193], v152 offset:33792
	ds_read_b128 v[194:197], v152 offset:34816
	ds_read_b128 v[198:201], v152 offset:35840
	ds_read_b128 v[202:205], v152 offset:36864
	ds_read_b128 v[206:209], v152 offset:37888
	ds_read_b128 v[210:213], v152 offset:38912
	ds_read_b128 v[214:217], v152 offset:39936
	global_load_lds_dwordx4 v[224:225], off
	v_lshl_add_u64 v[224:225], s[36:37], 0, v[134:135]
	s_mov_b32 m0, s43
	s_nop 0
	global_load_lds_dwordx4 v[224:225], off
	s_waitcnt vmcnt(8)
	s_waitcnt lgkmcnt(0)
	s_setprio 1
	s_barrier
	v_mfma_f32_16x16x32_bf16 v[126:129], v[154:157], v[186:189], v[126:129]
	v_mfma_f32_16x16x32_bf16 v[122:125], v[162:165], v[186:189], v[122:125]
	v_mfma_f32_16x16x32_bf16 v[118:121], v[154:157], v[194:197], v[118:121]
	v_mfma_f32_16x16x32_bf16 v[110:113], v[162:165], v[194:197], v[110:113]
	v_mfma_f32_16x16x32_bf16 v[102:105], v[154:157], v[202:205], v[102:105]
	v_mfma_f32_16x16x32_bf16 v[94:97], v[162:165], v[202:205], v[94:97]
	v_mfma_f32_16x16x32_bf16 v[86:89], v[154:157], v[210:213], v[86:89]
	v_mfma_f32_16x16x32_bf16 v[78:81], v[162:165], v[210:213], v[78:81]
	v_mfma_f32_16x16x32_bf16 v[126:129], v[158:161], v[190:193], v[126:129]
	v_mfma_f32_16x16x32_bf16 v[122:125], v[166:169], v[190:193], v[122:125]
	v_mfma_f32_16x16x32_bf16 v[118:121], v[158:161], v[198:201], v[118:121]
	v_mfma_f32_16x16x32_bf16 v[110:113], v[166:169], v[198:201], v[110:113]
	v_mfma_f32_16x16x32_bf16 v[102:105], v[158:161], v[206:209], v[102:105]
	v_mfma_f32_16x16x32_bf16 v[94:97], v[166:169], v[206:209], v[94:97]
	v_mfma_f32_16x16x32_bf16 v[86:89], v[158:161], v[214:217], v[86:89]
	v_mfma_f32_16x16x32_bf16 v[78:81], v[166:169], v[214:217], v[78:81]
	s_setprio 0
	s_setprio 1
	v_mfma_f32_16x16x32_bf16 v[114:117], v[170:173], v[186:189], v[114:117]
	v_mfma_f32_16x16x32_bf16 v[106:109], v[178:181], v[186:189], v[106:109]
	v_mfma_f32_16x16x32_bf16 v[98:101], v[170:173], v[194:197], v[98:101]
	v_mfma_f32_16x16x32_bf16 v[90:93], v[178:181], v[194:197], v[90:93]
	v_mfma_f32_16x16x32_bf16 v[82:85], v[170:173], v[202:205], v[82:85]
	v_mfma_f32_16x16x32_bf16 v[74:77], v[178:181], v[202:205], v[74:77]
	v_mfma_f32_16x16x32_bf16 v[70:73], v[170:173], v[210:213], v[70:73]
	v_mfma_f32_16x16x32_bf16 v[66:69], v[178:181], v[210:213], v[66:69]
	v_mfma_f32_16x16x32_bf16 v[114:117], v[174:177], v[190:193], v[114:117]
	v_mfma_f32_16x16x32_bf16 v[106:109], v[182:185], v[190:193], v[106:109]
	v_mfma_f32_16x16x32_bf16 v[98:101], v[174:177], v[198:201], v[98:101]
	v_mfma_f32_16x16x32_bf16 v[90:93], v[182:185], v[198:201], v[90:93]
	v_mfma_f32_16x16x32_bf16 v[82:85], v[174:177], v[206:209], v[82:85]
	v_mfma_f32_16x16x32_bf16 v[74:77], v[182:185], v[206:209], v[74:77]
	v_mfma_f32_16x16x32_bf16 v[70:73], v[174:177], v[214:217], v[70:73]
	v_mfma_f32_16x16x32_bf16 v[66:69], v[182:185], v[214:217], v[66:69]
	s_barrier
	s_setprio 0
	s_add_i32 s36, s60, s40
	v_lshl_add_u64 v[146:147], v[146:147], 0, s[10:11]
	s_mov_b32 m0, s36
	ds_read_b128 v[186:189], v152 offset:49152
	ds_read_b128 v[190:193], v152 offset:50176
	ds_read_b128 v[194:197], v152 offset:51200
	ds_read_b128 v[198:201], v152 offset:52224
	ds_read_b128 v[202:205], v152 offset:53248
	ds_read_b128 v[206:209], v152 offset:54272
	ds_read_b128 v[210:213], v152 offset:55296
	ds_read_b128 v[214:217], v152 offset:56320
	global_load_lds_dwordx4 v[146:147], off
	s_add_i32 m0, s36, 0x2000
	s_add_u32 s34, s34, 0x80080
	v_lshl_add_u64 v[146:147], v[218:219], 0, s[10:11]
	s_addc_u32 s35, s35, 0
	s_add_i32 s36, s61, s40
	global_load_lds_dwordx4 v[146:147], off
	v_lshl_add_u64 v[146:147], s[34:35], 0, v[132:133]
	s_mov_b32 m0, s36
	s_nop 0
	global_load_lds_dwordx4 v[146:147], off
	v_lshl_add_u64 v[146:147], s[34:35], 0, v[136:137]
	s_add_i32 m0, s36, 0x2000
	s_nop 0
	global_load_lds_dwordx4 v[146:147], off
	v_lshl_add_u64 v[146:147], v[220:221], 0, s[10:11]
	s_mov_b32 m0, s45
	s_nop 0
	global_load_lds_dwordx4 v[146:147], off
	v_lshl_add_u64 v[146:147], v[222:223], 0, s[10:11]
	s_mov_b32 m0, s46
	s_nop 0
	global_load_lds_dwordx4 v[146:147], off
	s_waitcnt vmcnt(8)
	s_waitcnt lgkmcnt(0)
	s_setprio 1
	s_barrier
	v_mfma_f32_16x16x32_bf16 v[62:65], v[154:157], v[186:189], v[62:65]
	v_mfma_f32_16x16x32_bf16 v[58:61], v[162:165], v[186:189], v[58:61]
	v_mfma_f32_16x16x32_bf16 v[54:57], v[154:157], v[194:197], v[54:57]
	v_mfma_f32_16x16x32_bf16 v[46:49], v[162:165], v[194:197], v[46:49]
	v_mfma_f32_16x16x32_bf16 v[38:41], v[154:157], v[202:205], v[38:41]
	v_mfma_f32_16x16x32_bf16 v[30:33], v[162:165], v[202:205], v[30:33]
	v_mfma_f32_16x16x32_bf16 v[22:25], v[154:157], v[210:213], v[22:25]
	v_mfma_f32_16x16x32_bf16 v[14:17], v[162:165], v[210:213], v[14:17]
	v_mfma_f32_16x16x32_bf16 v[62:65], v[158:161], v[190:193], v[62:65]
	v_mfma_f32_16x16x32_bf16 v[58:61], v[166:169], v[190:193], v[58:61]
	v_mfma_f32_16x16x32_bf16 v[54:57], v[158:161], v[198:201], v[54:57]
	v_mfma_f32_16x16x32_bf16 v[46:49], v[166:169], v[198:201], v[46:49]
	v_mfma_f32_16x16x32_bf16 v[38:41], v[158:161], v[206:209], v[38:41]
	v_mfma_f32_16x16x32_bf16 v[30:33], v[166:169], v[206:209], v[30:33]
	v_mfma_f32_16x16x32_bf16 v[22:25], v[158:161], v[214:217], v[22:25]
	v_mfma_f32_16x16x32_bf16 v[14:17], v[166:169], v[214:217], v[14:17]
	s_setprio 0
	s_setprio 1
	v_mfma_f32_16x16x32_bf16 v[50:53], v[170:173], v[186:189], v[50:53]
	v_mfma_f32_16x16x32_bf16 v[42:45], v[178:181], v[186:189], v[42:45]
	v_mfma_f32_16x16x32_bf16 v[34:37], v[170:173], v[194:197], v[34:37]
	v_mfma_f32_16x16x32_bf16 v[26:29], v[178:181], v[194:197], v[26:29]
	v_mfma_f32_16x16x32_bf16 v[18:21], v[170:173], v[202:205], v[18:21]
	v_mfma_f32_16x16x32_bf16 v[10:13], v[178:181], v[202:205], v[10:13]
	v_mfma_f32_16x16x32_bf16 v[6:9], v[170:173], v[210:213], v[6:9]
	v_mfma_f32_16x16x32_bf16 v[2:5], v[178:181], v[210:213], v[2:5]
	v_mfma_f32_16x16x32_bf16 v[50:53], v[174:177], v[190:193], v[50:53]
	v_mfma_f32_16x16x32_bf16 v[42:45], v[182:185], v[190:193], v[42:45]
	v_mfma_f32_16x16x32_bf16 v[34:37], v[174:177], v[198:201], v[34:37]
	v_mfma_f32_16x16x32_bf16 v[26:29], v[182:185], v[198:201], v[26:29]
	v_mfma_f32_16x16x32_bf16 v[18:21], v[174:177], v[206:209], v[18:21]
	v_mfma_f32_16x16x32_bf16 v[10:13], v[182:185], v[206:209], v[10:13]
	v_mfma_f32_16x16x32_bf16 v[6:9], v[174:177], v[214:217], v[6:9]
	v_mfma_f32_16x16x32_bf16 v[2:5], v[182:185], v[214:217], v[2:5]
	s_barrier
	s_setprio 0
	s_add_i32 s59, s59, 2
	s_add_u32 s30, s30, 0x100
	s_addc_u32 s31, s31, 0
	s_add_u32 s57, s57, 0x100
	s_addc_u32 s58, s58, 0
	s_cmp_gt_u32 s59, 29

.LBB0_1469:
	s_mov_b32 s100, 0
	s_cmp_lt_i32 s78, 10
	s_cselect_b64 s[4:5], -1, 0
	s_add_u32 s20, s86, 0x5b200000
	s_addc_u32 s21, s87, 0
	s_and_b64 s[0:1], s[4:5], s[0:1]
	s_andn2_b64 vcc, exec, s[0:1]
	s_cbranch_vccnz .LBB0_1486
	v_readlane_b32 s4, v254, 14
	s_cmpk_gt_i32 s4, 0x15ff
	v_readfirstlane_b32 s12, v0
	s_cbranch_scc1 .LBB0_1486
	v_lshrrev_b32_e32 v1, 5, v0
	v_lshrrev_b32_e32 v3, 1, v0
	v_and_b32_e32 v1, 4, v1
	v_bfe_u32 v2, v0, 2, 2
	v_and_b32_e32 v13, 24, v3
	v_or3_b32 v1, v1, v2, v13
	v_lshlrev_b32_e32 v2, 4, v0
	v_or_b32_e32 v10, 0x2000, v2
	s_add_u32 s15, s86, 0x2500000
	v_lshrrev_b32_e32 v3, 7, v10
	s_movk_i32 s4, 0x60
	v_readlane_b32 s6, v254, 14
	s_addc_u32 s33, s87, 0
	v_and_or_b32 v4, v3, s4, v1
	v_bfe_u32 v14, v0, 2, 4
	s_movk_i32 s4, 0x70
	s_ashr_i32 s37, s6, 31
	v_and_or_b32 v3, v3, s4, v14
	s_lshr_b32 s4, s37, 29
	s_add_i32 s4, s6, s4
	s_lshr_b32 s10, s12, 6
	s_ashr_i32 s5, s4, 3
	s_and_b32 s4, s4, -8
	s_lshr_b32 s9, s12, 8
	s_lshl_b32 s36, s10, 10
	s_sub_i32 s4, s6, s4
	s_cmp_lt_i32 s4, 0
	s_movk_i32 s38, 0x2c1
	s_cselect_b32 s6, s38, 0x2c0
	s_mul_i32 s4, s4, s6
	s_add_i32 s4, s4, s5
	s_mul_hi_i32 s5, s4, 0x2e8ba2e9
	s_lshr_b32 s6, s5, 31
	s_ashr_i32 s5, s5, 6
	s_add_i32 s5, s5, s6
	s_lshl_b32 s6, s5, 3
	s_mulk_i32 s5, 0x160
	s_sub_i32 s4, s4, s5
	s_sext_i32_i16 s5, s4
	s_bfe_u32 s5, s5, 0x3001c
	s_add_i32 s5, s4, s5
	s_sext_i32_i16 s7, s5
	s_and_b32 s5, s5, 0xfff8
	s_sub_i32 s4, s4, s5
	s_sext_i32_i16 s4, s4
	v_and_b32_e32 v5, 32, v0
	s_lshr_b32 s8, s7, 3
	s_add_i32 s26, s6, s4
	v_bitop3_b32 v11, v2, v5, 48 bitop3:0x6c
	v_and_b32_e32 v12, 64, v0
	s_ashr_i32 s27, s26, 31
	s_bfe_i64 s[6:7], s[8:9], 0x100000
	v_or_b32_e32 v2, v11, v12
	s_lshl_b64 s[4:5], s[26:27], 20
	s_lshl_b64 s[6:7], s[6:7], 20
	v_lshl_or_b32 v132, v3, 12, v2
	v_lshrrev_b32_e32 v3, 3, v0
	s_add_u32 s30, s15, s6
	v_and_or_b32 v1, v3, 32, v1
	s_addc_u32 s31, s33, s7
	s_add_i32 s39, s36, 0
	v_lshl_or_b32 v134, v1, 12, v2
	s_add_i32 m0, s39, 0x10000
	v_lshl_or_b32 v130, v4, 12, v2
	global_load_lds_dwordx4 v134, s[30:31]
	s_add_i32 m0, s39, 0x12000
	s_add_u32 s6, s30, 0x80000
	global_load_lds_dwordx4 v130, s[30:31]
	s_addc_u32 s7, s31, 0
	s_add_i32 m0, s39, 0x14000
	v_and_or_b32 v1, v3, 48, v14
	global_load_lds_dwordx4 v134, s[6:7]
	s_add_i32 m0, s39, 0x16000
	s_add_u32 s28, s20, s4
	s_addc_u32 s29, s21, s5
	s_add_i32 s40, s39, 0x2000
	v_lshl_or_b32 v136, v1, 12, v2
	global_load_lds_dwordx4 v130, s[6:7]
	s_mov_b32 m0, s39
	s_add_u32 s4, s28, 0x80000
	global_load_lds_dwordx4 v136, s[28:29]
	s_mov_b32 m0, s40
	s_addc_u32 s5, s29, 0
	s_add_i32 s41, s39, 0x4000
	global_load_lds_dwordx4 v132, s[28:29]
	s_mov_b32 m0, s41
	s_add_i32 s42, s39, 0x6000
	global_load_lds_dwordx4 v136, s[4:5]
	s_mov_b32 m0, s42
	v_mov_b32_e32 v135, 0
	global_load_lds_dwordx4 v132, s[4:5]
	v_mov_b32_e32 v131, v135
	v_mov_b32_e32 v137, v135
	v_mov_b32_e32 v133, v135
	s_cmp_eq_u32 s9, 1
	s_mov_b32 s43, 0
	v_lshl_add_u64 v[8:9], s[30:31], 0, v[134:135]
	v_lshl_add_u64 v[6:7], s[30:31], 0, v[130:131]
	v_lshl_add_u64 v[2:3], s[28:29], 0, v[136:137]
	s_cselect_b64 s[4:5], -1, 0
	s_cmp_lg_u32 s9, 1
	v_lshl_add_u64 v[4:5], s[28:29], 0, v[132:133]
	s_cbranch_scc1 .LBB0_1473
	s_barrier

.LBB0_1478:
	s_ashr_i32 s19, s18, 31
	s_lshl_b64 s[22:23], s[18:19], 20
	s_add_u32 s22, s20, s22
	s_addc_u32 s23, s21, s23
	s_and_b64 s[24:25], s[8:9], exec
	s_cselect_b32 s19, s23, s29
	s_cselect_b32 s27, s22, s28
	s_ashr_i32 s17, s16, 31
	s_lshl_b64 s[24:25], s[16:17], 20
	s_add_u32 s24, s15, s24
	s_addc_u32 s25, s33, s25
	s_and_b64 s[34:35], s[8:9], exec
	s_cselect_b32 s17, s25, s31
	s_cselect_b32 s51, s24, s30
	s_lshl_b32 s34, s26, 8
	s_ashr_i32 s35, s34, 31
	v_lshl_add_u64 v[238:239], s[34:35], 2, v[138:139]
	global_load_dword v240, v[238:239], off
	global_load_dword v242, v[238:239], off offset:64
	global_load_dword v244, v[238:239], off offset:128
	global_load_dword v246, v[238:239], off offset:192
	global_load_dword v248, v[238:239], off offset:512
	global_load_dword v250, v[238:239], off offset:576
	global_load_dword v252, v[238:239], off offset:640
	global_load_dword v238, v[238:239], off offset:704
	s_add_u32 s28, s28, 0x80080
	s_addc_u32 s29, s29, 0
	s_add_u32 s52, s30, 0x100
	s_addc_u32 s53, s31, 0
	s_mov_b32 s54, -2
	ds_read_b128 v[154:157], v150
	ds_read_b128 v[158:161], v150 offset:1024
	ds_read_b128 v[162:165], v150 offset:2048
	ds_read_b128 v[166:169], v150 offset:3072
	ds_read_b128 v[170:173], v151
	ds_read_b128 v[174:177], v151 offset:1024
	ds_read_b128 v[178:181], v151 offset:2048
	ds_read_b128 v[182:185], v151 offset:3072
	s_add_u32 s30, s28, 0xfff80080
	s_addc_u32 s31, s29, -1
	s_cmp_eq_u32 s54, 28
	s_cselect_b32 s35, s19, s31
	s_cselect_b32 s34, s27, s30
	s_cselect_b32 s31, s17, s53
	s_cselect_b32 s30, s51, s52
	v_lshl_add_u64 v[218:219], s[28:29], 0, v[140:141]
	s_add_i32 m0, s39, 0xc000
	ds_read_b128 v[186:189], v152
	ds_read_b128 v[190:193], v152 offset:1024
	ds_read_b128 v[194:197], v152 offset:2048
	ds_read_b128 v[198:201], v152 offset:3072
	ds_read_b128 v[202:205], v152 offset:4096
	ds_read_b128 v[206:209], v152 offset:5120
	ds_read_b128 v[210:213], v152 offset:6144
	ds_read_b128 v[214:217], v152 offset:7168
	global_load_lds_dwordx4 v[218:219], off
	v_lshl_add_u64 v[218:219], s[28:29], 0, v[142:143]
	s_add_i32 m0, s39, 0xe000
	s_nop 0
	global_load_lds_dwordx4 v[218:219], off
	s_cmp_lg_u32 s100, 0
	s_cbranch_scc1 .Lrx_1479_0
	s_waitcnt vmcnt(8)
.Lrx_1479_0:
	s_waitcnt vmcnt(24)
	s_waitcnt lgkmcnt(0)
	s_setprio 1
	s_barrier
	v_mfma_f32_16x16x32_bf16 v[126:129], v[154:157], v[186:189], 0
	v_mfma_f32_16x16x32_bf16 v[122:125], v[162:165], v[186:189], 0
	v_mfma_f32_16x16x32_bf16 v[118:121], v[154:157], v[194:197], 0
	v_mfma_f32_16x16x32_bf16 v[114:117], v[162:165], v[194:197], 0
	v_mfma_f32_16x16x32_bf16 v[110:113], v[154:157], v[202:205], 0
	v_mfma_f32_16x16x32_bf16 v[102:105], v[162:165], v[202:205], 0
	v_mfma_f32_16x16x32_bf16 v[94:97], v[154:157], v[210:213], 0
	v_mfma_f32_16x16x32_bf16 v[86:89], v[162:165], v[210:213], 0
	v_mfma_f32_16x16x32_bf16 v[126:129], v[158:161], v[190:193], v[126:129]
	v_mfma_f32_16x16x32_bf16 v[122:125], v[166:169], v[190:193], v[122:125]
	v_mfma_f32_16x16x32_bf16 v[118:121], v[158:161], v[198:201], v[118:121]
	v_mfma_f32_16x16x32_bf16 v[114:117], v[166:169], v[198:201], v[114:117]
	v_mfma_f32_16x16x32_bf16 v[110:113], v[158:161], v[206:209], v[110:113]
	v_mfma_f32_16x16x32_bf16 v[102:105], v[166:169], v[206:209], v[102:105]
	v_mfma_f32_16x16x32_bf16 v[94:97], v[158:161], v[214:217], v[94:97]
	v_mfma_f32_16x16x32_bf16 v[86:89], v[166:169], v[214:217], v[86:89]
	s_setprio 0
	s_setprio 1
	v_mfma_f32_16x16x32_bf16 v[106:109], v[170:173], v[186:189], 0
	v_mfma_f32_16x16x32_bf16 v[98:101], v[178:181], v[186:189], 0
	v_mfma_f32_16x16x32_bf16 v[90:93], v[170:173], v[194:197], 0
	v_mfma_f32_16x16x32_bf16 v[82:85], v[178:181], v[194:197], 0
	v_mfma_f32_16x16x32_bf16 v[78:81], v[170:173], v[202:205], 0
	v_mfma_f32_16x16x32_bf16 v[74:77], v[178:181], v[202:205], 0
	v_mfma_f32_16x16x32_bf16 v[70:73], v[170:173], v[210:213], 0
	v_mfma_f32_16x16x32_bf16 v[66:69], v[178:181], v[210:213], 0
	v_mfma_f32_16x16x32_bf16 v[106:109], v[174:177], v[190:193], v[106:109]
	v_mfma_f32_16x16x32_bf16 v[98:101], v[182:185], v[190:193], v[98:101]
	v_mfma_f32_16x16x32_bf16 v[90:93], v[174:177], v[198:201], v[90:93]
	v_mfma_f32_16x16x32_bf16 v[82:85], v[182:185], v[198:201], v[82:85]
	v_mfma_f32_16x16x32_bf16 v[78:81], v[174:177], v[206:209], v[78:81]
	v_mfma_f32_16x16x32_bf16 v[74:77], v[182:185], v[206:209], v[74:77]
	v_mfma_f32_16x16x32_bf16 v[70:73], v[174:177], v[214:217], v[70:73]
	v_mfma_f32_16x16x32_bf16 v[66:69], v[182:185], v[214:217], v[66:69]
	s_barrier
	s_setprio 0
	s_add_i32 s55, s47, s36
	v_lshl_add_u64 v[218:219], s[30:31], 0, v[134:135]
	s_mov_b32 m0, s55
	ds_read_b128 v[186:189], v152 offset:16384
	ds_read_b128 v[190:193], v152 offset:17408
	ds_read_b128 v[194:197], v152 offset:18432
	ds_read_b128 v[198:201], v152 offset:19456
	ds_read_b128 v[202:205], v152 offset:20480
	ds_read_b128 v[206:209], v152 offset:21504
	ds_read_b128 v[210:213], v152 offset:22528
	ds_read_b128 v[214:217], v152 offset:23552
	global_load_lds_dwordx4 v[218:219], off
	s_add_i32 m0, s55, 0x2000
	s_add_u32 s56, s30, 0x80000
	v_lshl_add_u64 v[220:221], s[30:31], 0, v[130:131]
	s_addc_u32 s57, s31, 0
	s_add_i32 s55, s48, s36
	global_load_lds_dwordx4 v[220:221], off
	v_lshl_add_u64 v[222:223], s[56:57], 0, v[134:135]
	s_mov_b32 m0, s55
	v_lshl_add_u64 v[224:225], s[34:35], 0, v[132:133]
	global_load_lds_dwordx4 v[222:223], off
	v_lshl_add_u64 v[222:223], s[56:57], 0, v[130:131]
	s_add_i32 m0, s55, 0x2000
	s_nop 0
	global_load_lds_dwordx4 v[222:223], off
	v_lshl_add_u64 v[222:223], s[34:35], 0, v[136:137]
	s_mov_b32 m0, s39
	s_nop 0
	global_load_lds_dwordx4 v[222:223], off
	s_mov_b32 m0, s40
	s_nop 0
	global_load_lds_dwordx4 v[224:225], off
	s_cmp_lg_u32 s100, 0
	s_cbranch_scc1 .Lrx_1479_1
	s_waitcnt vmcnt(8)
.Lrx_1479_1:
	s_waitcnt vmcnt(24)
	s_mov_b32 s100, 1
	s_waitcnt lgkmcnt(0)
	s_setprio 1
	s_barrier
	v_mfma_f32_16x16x32_bf16 v[62:65], v[154:157], v[186:189], 0
	v_mfma_f32_16x16x32_bf16 v[58:61], v[162:165], v[186:189], 0
	v_mfma_f32_16x16x32_bf16 v[54:57], v[154:157], v[194:197], 0
	v_mfma_f32_16x16x32_bf16 v[50:53], v[162:165], v[194:197], 0
	v_mfma_f32_16x16x32_bf16 v[46:49], v[154:157], v[202:205], 0
	v_mfma_f32_16x16x32_bf16 v[38:41], v[162:165], v[202:205], 0
	v_mfma_f32_16x16x32_bf16 v[30:33], v[154:157], v[210:213], 0
	v_mfma_f32_16x16x32_bf16 v[22:25], v[162:165], v[210:213], 0
	v_mfma_f32_16x16x32_bf16 v[62:65], v[158:161], v[190:193], v[62:65]
	v_mfma_f32_16x16x32_bf16 v[58:61], v[166:169], v[190:193], v[58:61]
	v_mfma_f32_16x16x32_bf16 v[54:57], v[158:161], v[198:201], v[54:57]
	v_mfma_f32_16x16x32_bf16 v[50:53], v[166:169], v[198:201], v[50:53]
	v_mfma_f32_16x16x32_bf16 v[46:49], v[158:161], v[206:209], v[46:49]
	v_mfma_f32_16x16x32_bf16 v[38:41], v[166:169], v[206:209], v[38:41]
	v_mfma_f32_16x16x32_bf16 v[30:33], v[158:161], v[214:217], v[30:33]
	v_mfma_f32_16x16x32_bf16 v[22:25], v[166:169], v[214:217], v[22:25]
	s_setprio 0
	s_setprio 1
	v_mfma_f32_16x16x32_bf16 v[42:45], v[170:173], v[186:189], 0
	v_mfma_f32_16x16x32_bf16 v[34:37], v[178:181], v[186:189], 0
	v_mfma_f32_16x16x32_bf16 v[26:29], v[170:173], v[194:197], 0
	v_mfma_f32_16x16x32_bf16 v[18:21], v[178:181], v[194:197], 0
	v_mfma_f32_16x16x32_bf16 v[14:17], v[170:173], v[202:205], 0
	v_mfma_f32_16x16x32_bf16 v[10:13], v[178:181], v[202:205], 0
	v_mfma_f32_16x16x32_bf16 v[6:9], v[170:173], v[210:213], 0
	v_mfma_f32_16x16x32_bf16 v[2:5], v[178:181], v[210:213], 0
	v_mfma_f32_16x16x32_bf16 v[42:45], v[174:177], v[190:193], v[42:45]
	v_mfma_f32_16x16x32_bf16 v[34:37], v[182:185], v[190:193], v[34:37]
	v_mfma_f32_16x16x32_bf16 v[26:29], v[174:177], v[198:201], v[26:29]
	v_mfma_f32_16x16x32_bf16 v[18:21], v[182:185], v[198:201], v[18:21]
	v_mfma_f32_16x16x32_bf16 v[14:17], v[174:177], v[206:209], v[14:17]
	v_mfma_f32_16x16x32_bf16 v[10:13], v[182:185], v[206:209], v[10:13]
	v_mfma_f32_16x16x32_bf16 v[6:9], v[174:177], v[214:217], v[6:9]
	v_mfma_f32_16x16x32_bf16 v[2:5], v[182:185], v[214:217], v[2:5]
	s_barrier
	s_setprio 0
	s_add_i32 s55, 0, 0x18000
	v_add_u32_e32 v153, s55, v148
	s_add_i32 s56, 0, 0x1c000
	ds_read_b128 v[154:157], v153
	ds_read_b128 v[158:161], v153 offset:1024
	ds_read_b128 v[162:165], v153 offset:2048
	ds_read_b128 v[166:169], v153 offset:3072
	v_add_u32_e32 v153, s56, v148
	ds_read_b128 v[170:173], v153
	ds_read_b128 v[174:177], v153 offset:1024
	ds_read_b128 v[178:181], v153 offset:2048
	ds_read_b128 v[182:185], v153 offset:3072
	s_add_u32 s34, s34, 0x80000
	s_addc_u32 s35, s35, 0
	s_mov_b32 m0, s41
	v_lshl_add_u64 v[226:227], s[34:35], 0, v[136:137]
	ds_read_b128 v[186:189], v152 offset:32768
	ds_read_b128 v[190:193], v152 offset:33792
	ds_read_b128 v[194:197], v152 offset:34816
	ds_read_b128 v[198:201], v152 offset:35840
	ds_read_b128 v[202:205], v152 offset:36864
	ds_read_b128 v[206:209], v152 offset:37888
	ds_read_b128 v[210:213], v152 offset:38912
	ds_read_b128 v[214:217], v152 offset:39936
	global_load_lds_dwordx4 v[226:227], off
	v_lshl_add_u64 v[226:227], s[34:35], 0, v[132:133]
	s_mov_b32 m0, s42
	s_nop 0
	global_load_lds_dwordx4 v[226:227], off
	s_waitcnt vmcnt(8)
	s_waitcnt lgkmcnt(0)
	s_setprio 1
	s_barrier
	v_mfma_f32_16x16x32_bf16 v[126:129], v[154:157], v[186:189], v[126:129]
	v_mfma_f32_16x16x32_bf16 v[122:125], v[162:165], v[186:189], v[122:125]
	v_mfma_f32_16x16x32_bf16 v[118:121], v[154:157], v[194:197], v[118:121]
	v_mfma_f32_16x16x32_bf16 v[114:117], v[162:165], v[194:197], v[114:117]
	v_mfma_f32_16x16x32_bf16 v[110:113], v[154:157], v[202:205], v[110:113]
	v_mfma_f32_16x16x32_bf16 v[102:105], v[162:165], v[202:205], v[102:105]
	v_mfma_f32_16x16x32_bf16 v[94:97], v[154:157], v[210:213], v[94:97]
	v_mfma_f32_16x16x32_bf16 v[86:89], v[162:165], v[210:213], v[86:89]
	v_mfma_f32_16x16x32_bf16 v[126:129], v[158:161], v[190:193], v[126:129]
	v_mfma_f32_16x16x32_bf16 v[122:125], v[166:169], v[190:193], v[122:125]
	v_mfma_f32_16x16x32_bf16 v[118:121], v[158:161], v[198:201], v[118:121]
	v_mfma_f32_16x16x32_bf16 v[114:117], v[166:169], v[198:201], v[114:117]
	v_mfma_f32_16x16x32_bf16 v[110:113], v[158:161], v[206:209], v[110:113]
	v_mfma_f32_16x16x32_bf16 v[102:105], v[166:169], v[206:209], v[102:105]
	v_mfma_f32_16x16x32_bf16 v[94:97], v[158:161], v[214:217], v[94:97]
	v_mfma_f32_16x16x32_bf16 v[86:89], v[166:169], v[214:217], v[86:89]
	s_setprio 0
	s_setprio 1
	v_mfma_f32_16x16x32_bf16 v[106:109], v[170:173], v[186:189], v[106:109]
	v_mfma_f32_16x16x32_bf16 v[98:101], v[178:181], v[186:189], v[98:101]
	v_mfma_f32_16x16x32_bf16 v[90:93], v[170:173], v[194:197], v[90:93]
	v_mfma_f32_16x16x32_bf16 v[82:85], v[178:181], v[194:197], v[82:85]
	v_mfma_f32_16x16x32_bf16 v[78:81], v[170:173], v[202:205], v[78:81]
	v_mfma_f32_16x16x32_bf16 v[74:77], v[178:181], v[202:205], v[74:77]
	v_mfma_f32_16x16x32_bf16 v[70:73], v[170:173], v[210:213], v[70:73]
	v_mfma_f32_16x16x32_bf16 v[66:69], v[178:181], v[210:213], v[66:69]
	v_mfma_f32_16x16x32_bf16 v[106:109], v[174:177], v[190:193], v[106:109]
	v_mfma_f32_16x16x32_bf16 v[98:101], v[182:185], v[190:193], v[98:101]
	v_mfma_f32_16x16x32_bf16 v[90:93], v[174:177], v[198:201], v[90:93]
	v_mfma_f32_16x16x32_bf16 v[82:85], v[182:185], v[198:201], v[82:85]
	v_mfma_f32_16x16x32_bf16 v[78:81], v[174:177], v[206:209], v[78:81]
	v_mfma_f32_16x16x32_bf16 v[74:77], v[182:185], v[206:209], v[74:77]
	v_mfma_f32_16x16x32_bf16 v[70:73], v[174:177], v[214:217], v[70:73]
	v_mfma_f32_16x16x32_bf16 v[66:69], v[182:185], v[214:217], v[66:69]
	s_barrier
	s_setprio 0
	s_add_i32 s34, s55, s36
	v_lshl_add_u64 v[218:219], v[218:219], 0, s[10:11]
	s_mov_b32 m0, s34
	ds_read_b128 v[186:189], v152 offset:49152
	ds_read_b128 v[190:193], v152 offset:50176
	ds_read_b128 v[194:197], v152 offset:51200
	ds_read_b128 v[198:201], v152 offset:52224
	ds_read_b128 v[202:205], v152 offset:53248
	ds_read_b128 v[206:209], v152 offset:54272
	ds_read_b128 v[210:213], v152 offset:55296
	ds_read_b128 v[214:217], v152 offset:56320
	global_load_lds_dwordx4 v[218:219], off
	s_add_i32 m0, s34, 0x2000
	s_add_u32 s30, s30, 0x80080
	v_lshl_add_u64 v[218:219], v[220:221], 0, s[10:11]
	s_addc_u32 s31, s31, 0
	s_add_i32 s34, s56, s36
	global_load_lds_dwordx4 v[218:219], off
	v_lshl_add_u64 v[218:219], s[30:31], 0, v[134:135]
	s_mov_b32 m0, s34
	s_nop 0
	global_load_lds_dwordx4 v[218:219], off
	v_lshl_add_u64 v[218:219], s[30:31], 0, v[130:131]
	s_add_i32 m0, s34, 0x2000
	s_nop 0
	global_load_lds_dwordx4 v[218:219], off
	v_lshl_add_u64 v[218:219], v[222:223], 0, s[10:11]
	s_mov_b32 m0, s44
	s_nop 0
	global_load_lds_dwordx4 v[218:219], off
	v_lshl_add_u64 v[218:219], v[224:225], 0, s[10:11]
	s_mov_b32 m0, s45
	s_nop 0
	global_load_lds_dwordx4 v[218:219], off
	s_waitcnt vmcnt(8)
	s_waitcnt lgkmcnt(0)
	s_setprio 1
	s_barrier
	v_mfma_f32_16x16x32_bf16 v[62:65], v[154:157], v[186:189], v[62:65]
	v_mfma_f32_16x16x32_bf16 v[58:61], v[162:165], v[186:189], v[58:61]
	v_mfma_f32_16x16x32_bf16 v[54:57], v[154:157], v[194:197], v[54:57]
	v_mfma_f32_16x16x32_bf16 v[50:53], v[162:165], v[194:197], v[50:53]
	v_mfma_f32_16x16x32_bf16 v[46:49], v[154:157], v[202:205], v[46:49]
	v_mfma_f32_16x16x32_bf16 v[38:41], v[162:165], v[202:205], v[38:41]
	v_mfma_f32_16x16x32_bf16 v[30:33], v[154:157], v[210:213], v[30:33]
	v_mfma_f32_16x16x32_bf16 v[22:25], v[162:165], v[210:213], v[22:25]
	v_mfma_f32_16x16x32_bf16 v[62:65], v[158:161], v[190:193], v[62:65]
	v_mfma_f32_16x16x32_bf16 v[58:61], v[166:169], v[190:193], v[58:61]
	v_mfma_f32_16x16x32_bf16 v[54:57], v[158:161], v[198:201], v[54:57]
	v_mfma_f32_16x16x32_bf16 v[50:53], v[166:169], v[198:201], v[50:53]
	v_mfma_f32_16x16x32_bf16 v[46:49], v[158:161], v[206:209], v[46:49]
	v_mfma_f32_16x16x32_bf16 v[38:41], v[166:169], v[206:209], v[38:41]
	v_mfma_f32_16x16x32_bf16 v[30:33], v[158:161], v[214:217], v[30:33]
	v_mfma_f32_16x16x32_bf16 v[22:25], v[166:169], v[214:217], v[22:25]
	s_setprio 0
	s_setprio 1
	v_mfma_f32_16x16x32_bf16 v[42:45], v[170:173], v[186:189], v[42:45]
	v_mfma_f32_16x16x32_bf16 v[34:37], v[178:181], v[186:189], v[34:37]
	v_mfma_f32_16x16x32_bf16 v[26:29], v[170:173], v[194:197], v[26:29]
	v_mfma_f32_16x16x32_bf16 v[18:21], v[178:181], v[194:197], v[18:21]
	v_mfma_f32_16x16x32_bf16 v[14:17], v[170:173], v[202:205], v[14:17]
	v_mfma_f32_16x16x32_bf16 v[10:13], v[178:181], v[202:205], v[10:13]
	v_mfma_f32_16x16x32_bf16 v[6:9], v[170:173], v[210:213], v[6:9]
	v_mfma_f32_16x16x32_bf16 v[2:5], v[178:181], v[210:213], v[2:5]
	v_mfma_f32_16x16x32_bf16 v[42:45], v[174:177], v[190:193], v[42:45]
	v_mfma_f32_16x16x32_bf16 v[34:37], v[182:185], v[190:193], v[34:37]
	v_mfma_f32_16x16x32_bf16 v[26:29], v[174:177], v[198:201], v[26:29]
	v_mfma_f32_16x16x32_bf16 v[18:21], v[182:185], v[198:201], v[18:21]
	v_mfma_f32_16x16x32_bf16 v[14:17], v[174:177], v[206:209], v[14:17]
	v_mfma_f32_16x16x32_bf16 v[10:13], v[182:185], v[206:209], v[10:13]
	v_mfma_f32_16x16x32_bf16 v[6:9], v[174:177], v[214:217], v[6:9]
	v_mfma_f32_16x16x32_bf16 v[2:5], v[182:185], v[214:217], v[2:5]
	s_barrier
	s_setprio 0
	s_add_i32 s54, s54, 2
	s_add_u32 s28, s28, 0x100
	s_addc_u32 s29, s29, 0
	s_add_u32 s52, s52, 0x100
	s_addc_u32 s53, s53, 0
	s_cmp_gt_u32 s54, 29

.LBB0_1540:
	s_mov_b32 s100, 0
	s_cmp_lt_i32 s78, 11
	s_cselect_b64 s[0:1], -1, 0
	s_and_b64 s[4:5], s[0:1], s[4:5]
	s_andn2_b64 vcc, exec, s[4:5]
	s_cbranch_vccnz .LBB0_1569
	v_readlane_b32 s0, v254, 14
	s_cmpk_gt_i32 s0, 0x3ff
	v_readfirstlane_b32 s8, v0
	s_cbranch_scc1 .LBB0_1569
	v_readlane_b32 s1, v254, 14
	s_ashr_i32 s33, s1, 31
	s_lshr_b32 s0, s33, 29
	s_add_i32 s7, s1, s0
	s_and_b32 s0, s7, -8
	s_sub_i32 s9, s1, s0
	s_cmp_gt_i32 s9, -1
	s_cbranch_scc0 .LBB0_1544
	s_lshl_b32 s6, s9, 7
	s_cbranch_execz .LBB0_1545
	s_branch .LBB0_1546

.LBB0_1561:
	s_add_u32 s26, s26, 0x160080
	s_addc_u32 s27, s27, 0
	s_add_u32 s57, s28, 0x100
	s_addc_u32 s58, s29, 0
	s_mov_b32 s59, -2
	ds_read_b128 v[154:157], v150
	ds_read_b128 v[158:161], v150 offset:1024
	ds_read_b128 v[162:165], v150 offset:2048
	ds_read_b128 v[166:169], v150 offset:3072
	ds_read_b128 v[170:173], v151
	ds_read_b128 v[174:177], v151 offset:1024
	ds_read_b128 v[178:181], v151 offset:2048
	ds_read_b128 v[182:185], v151 offset:3072
	s_add_u32 s28, s26, 0xffea0080
	s_addc_u32 s29, s27, -1
	s_cmpk_eq_i32 s59, 0x54
	s_cselect_b32 s31, s1, s29
	s_cselect_b32 s30, s0, s28
	s_cselect_b32 s29, s25, s58
	s_cselect_b32 s28, s24, s57
	v_lshl_add_u64 v[146:147], s[26:27], 0, v[138:139]
	s_add_i32 m0, s39, 0xc000
	ds_read_b128 v[186:189], v152
	ds_read_b128 v[190:193], v152 offset:1024
	ds_read_b128 v[194:197], v152 offset:2048
	ds_read_b128 v[198:201], v152 offset:3072
	ds_read_b128 v[202:205], v152 offset:4096
	ds_read_b128 v[206:209], v152 offset:5120
	ds_read_b128 v[210:213], v152 offset:6144
	ds_read_b128 v[214:217], v152 offset:7168
	global_load_lds_dwordx4 v[146:147], off
	v_lshl_add_u64 v[146:147], s[26:27], 0, v[140:141]
	s_add_i32 m0, s39, 0xe000
	s_nop 0
	global_load_lds_dwordx4 v[146:147], off
	s_cmp_lg_u32 s100, 0
	s_cbranch_scc1 .Lrx_1562_0
	s_waitcnt vmcnt(8)
.Lrx_1562_0:
	s_waitcnt vmcnt(24)
	s_waitcnt lgkmcnt(0)
	s_setprio 1
	s_barrier
	v_mfma_f32_16x16x32_bf16 v[126:129], v[154:157], v[186:189], 0
	v_mfma_f32_16x16x32_bf16 v[122:125], v[162:165], v[186:189], 0
	v_mfma_f32_16x16x32_bf16 v[118:121], v[154:157], v[194:197], 0
	v_mfma_f32_16x16x32_bf16 v[110:113], v[162:165], v[194:197], 0
	v_mfma_f32_16x16x32_bf16 v[102:105], v[154:157], v[202:205], 0
	v_mfma_f32_16x16x32_bf16 v[94:97], v[162:165], v[202:205], 0
	v_mfma_f32_16x16x32_bf16 v[86:89], v[154:157], v[210:213], 0
	v_mfma_f32_16x16x32_bf16 v[78:81], v[162:165], v[210:213], 0
	v_mfma_f32_16x16x32_bf16 v[126:129], v[158:161], v[190:193], v[126:129]
	v_mfma_f32_16x16x32_bf16 v[122:125], v[166:169], v[190:193], v[122:125]
	v_mfma_f32_16x16x32_bf16 v[118:121], v[158:161], v[198:201], v[118:121]
	v_mfma_f32_16x16x32_bf16 v[110:113], v[166:169], v[198:201], v[110:113]
	v_mfma_f32_16x16x32_bf16 v[102:105], v[158:161], v[206:209], v[102:105]
	v_mfma_f32_16x16x32_bf16 v[94:97], v[166:169], v[206:209], v[94:97]
	v_mfma_f32_16x16x32_bf16 v[86:89], v[158:161], v[214:217], v[86:89]
	v_mfma_f32_16x16x32_bf16 v[78:81], v[166:169], v[214:217], v[78:81]
	s_setprio 0
	s_setprio 1
	v_mfma_f32_16x16x32_bf16 v[114:117], v[170:173], v[186:189], 0
	v_mfma_f32_16x16x32_bf16 v[106:109], v[178:181], v[186:189], 0
	v_mfma_f32_16x16x32_bf16 v[98:101], v[170:173], v[194:197], 0
	v_mfma_f32_16x16x32_bf16 v[90:93], v[178:181], v[194:197], 0
	v_mfma_f32_16x16x32_bf16 v[82:85], v[170:173], v[202:205], 0
	v_mfma_f32_16x16x32_bf16 v[74:77], v[178:181], v[202:205], 0
	v_mfma_f32_16x16x32_bf16 v[70:73], v[170:173], v[210:213], 0
	v_mfma_f32_16x16x32_bf16 v[66:69], v[178:181], v[210:213], 0
	v_mfma_f32_16x16x32_bf16 v[114:117], v[174:177], v[190:193], v[114:117]
	v_mfma_f32_16x16x32_bf16 v[106:109], v[182:185], v[190:193], v[106:109]
	v_mfma_f32_16x16x32_bf16 v[98:101], v[174:177], v[198:201], v[98:101]
	v_mfma_f32_16x16x32_bf16 v[90:93], v[182:185], v[198:201], v[90:93]
	v_mfma_f32_16x16x32_bf16 v[82:85], v[174:177], v[206:209], v[82:85]
	v_mfma_f32_16x16x32_bf16 v[74:77], v[182:185], v[206:209], v[74:77]
	v_mfma_f32_16x16x32_bf16 v[70:73], v[174:177], v[214:217], v[70:73]
	v_mfma_f32_16x16x32_bf16 v[66:69], v[182:185], v[214:217], v[66:69]
	s_barrier
	s_setprio 0
	s_add_i32 s60, s47, s38
	v_lshl_add_u64 v[146:147], s[28:29], 0, v[132:133]
	s_mov_b32 m0, s60
	ds_read_b128 v[186:189], v152 offset:16384
	ds_read_b128 v[190:193], v152 offset:17408
	ds_read_b128 v[194:197], v152 offset:18432
	ds_read_b128 v[198:201], v152 offset:19456
	ds_read_b128 v[202:205], v152 offset:20480
	ds_read_b128 v[206:209], v152 offset:21504
	ds_read_b128 v[210:213], v152 offset:22528
	ds_read_b128 v[214:217], v152 offset:23552
	global_load_lds_dwordx4 v[146:147], off
	s_add_i32 m0, s60, 0x2000
	s_add_u32 s60, s28, 0x160000
	v_lshl_add_u64 v[218:219], s[28:29], 0, v[136:137]
	s_addc_u32 s61, s29, 0
	s_add_i32 s62, s48, s38
	global_load_lds_dwordx4 v[218:219], off
	v_lshl_add_u64 v[220:221], s[60:61], 0, v[132:133]
	s_mov_b32 m0, s62
	v_lshl_add_u64 v[222:223], s[30:31], 0, v[134:135]
	global_load_lds_dwordx4 v[220:221], off
	v_lshl_add_u64 v[220:221], s[60:61], 0, v[136:137]
	s_add_i32 m0, s62, 0x2000
	s_nop 0
	global_load_lds_dwordx4 v[220:221], off
	v_lshl_add_u64 v[220:221], s[30:31], 0, v[130:131]
	s_mov_b32 m0, s39
	s_nop 0
	global_load_lds_dwordx4 v[220:221], off
	s_mov_b32 m0, s40
	s_nop 0
	global_load_lds_dwordx4 v[222:223], off
	s_cmp_lg_u32 s100, 0
	s_cbranch_scc1 .Lrx_1562_1
	s_waitcnt vmcnt(8)
.Lrx_1562_1:
	s_waitcnt vmcnt(24)
	s_mov_b32 s100, 1
	s_waitcnt lgkmcnt(0)
	s_setprio 1
	s_barrier
	v_mfma_f32_16x16x32_bf16 v[62:65], v[154:157], v[186:189], 0
	v_mfma_f32_16x16x32_bf16 v[58:61], v[162:165], v[186:189], 0
	v_mfma_f32_16x16x32_bf16 v[54:57], v[154:157], v[194:197], 0
	v_mfma_f32_16x16x32_bf16 v[46:49], v[162:165], v[194:197], 0
	v_mfma_f32_16x16x32_bf16 v[38:41], v[154:157], v[202:205], 0
	v_mfma_f32_16x16x32_bf16 v[30:33], v[162:165], v[202:205], 0
	v_mfma_f32_16x16x32_bf16 v[22:25], v[154:157], v[210:213], 0
	v_mfma_f32_16x16x32_bf16 v[14:17], v[162:165], v[210:213], 0
	v_mfma_f32_16x16x32_bf16 v[62:65], v[158:161], v[190:193], v[62:65]
	v_mfma_f32_16x16x32_bf16 v[58:61], v[166:169], v[190:193], v[58:61]
	v_mfma_f32_16x16x32_bf16 v[54:57], v[158:161], v[198:201], v[54:57]
	v_mfma_f32_16x16x32_bf16 v[46:49], v[166:169], v[198:201], v[46:49]
	v_mfma_f32_16x16x32_bf16 v[38:41], v[158:161], v[206:209], v[38:41]
	v_mfma_f32_16x16x32_bf16 v[30:33], v[166:169], v[206:209], v[30:33]
	v_mfma_f32_16x16x32_bf16 v[22:25], v[158:161], v[214:217], v[22:25]
	v_mfma_f32_16x16x32_bf16 v[14:17], v[166:169], v[214:217], v[14:17]
	s_setprio 0
	s_setprio 1
	v_mfma_f32_16x16x32_bf16 v[50:53], v[170:173], v[186:189], 0
	v_mfma_f32_16x16x32_bf16 v[42:45], v[178:181], v[186:189], 0
	v_mfma_f32_16x16x32_bf16 v[34:37], v[170:173], v[194:197], 0
	v_mfma_f32_16x16x32_bf16 v[26:29], v[178:181], v[194:197], 0
	v_mfma_f32_16x16x32_bf16 v[18:21], v[170:173], v[202:205], 0
	v_mfma_f32_16x16x32_bf16 v[10:13], v[178:181], v[202:205], 0
	v_mfma_f32_16x16x32_bf16 v[6:9], v[170:173], v[210:213], 0
	v_mfma_f32_16x16x32_bf16 v[2:5], v[178:181], v[210:213], 0
	v_mfma_f32_16x16x32_bf16 v[50:53], v[174:177], v[190:193], v[50:53]
	v_mfma_f32_16x16x32_bf16 v[42:45], v[182:185], v[190:193], v[42:45]
	v_mfma_f32_16x16x32_bf16 v[34:37], v[174:177], v[198:201], v[34:37]
	v_mfma_f32_16x16x32_bf16 v[26:29], v[182:185], v[198:201], v[26:29]
	v_mfma_f32_16x16x32_bf16 v[18:21], v[174:177], v[206:209], v[18:21]
	v_mfma_f32_16x16x32_bf16 v[10:13], v[182:185], v[206:209], v[10:13]
	v_mfma_f32_16x16x32_bf16 v[6:9], v[174:177], v[214:217], v[6:9]
	v_mfma_f32_16x16x32_bf16 v[2:5], v[182:185], v[214:217], v[2:5]
	s_barrier
	s_setprio 0
	s_add_i32 s60, 0, 0x18000
	v_add_u32_e32 v153, s60, v148
	s_add_i32 s61, 0, 0x1c000
	ds_read_b128 v[154:157], v153
	ds_read_b128 v[158:161], v153 offset:1024
	ds_read_b128 v[162:165], v153 offset:2048
	ds_read_b128 v[166:169], v153 offset:3072
	v_add_u32_e32 v153, s61, v148
	ds_read_b128 v[170:173], v153
	ds_read_b128 v[174:177], v153 offset:1024
	ds_read_b128 v[178:181], v153 offset:2048
	ds_read_b128 v[182:185], v153 offset:3072
	s_add_u32 s30, s30, 0x160000
	s_addc_u32 s31, s31, 0
	s_mov_b32 m0, s41
	v_lshl_add_u64 v[224:225], s[30:31], 0, v[130:131]
	ds_read_b128 v[186:189], v152 offset:32768
	ds_read_b128 v[190:193], v152 offset:33792
	ds_read_b128 v[194:197], v152 offset:34816
	ds_read_b128 v[198:201], v152 offset:35840
	ds_read_b128 v[202:205], v152 offset:36864
	ds_read_b128 v[206:209], v152 offset:37888
	ds_read_b128 v[210:213], v152 offset:38912
	ds_read_b128 v[214:217], v152 offset:39936
	global_load_lds_dwordx4 v[224:225], off
	v_lshl_add_u64 v[224:225], s[30:31], 0, v[134:135]
	s_mov_b32 m0, s42
	s_nop 0
	global_load_lds_dwordx4 v[224:225], off
	s_waitcnt vmcnt(8)
	s_waitcnt lgkmcnt(0)
	s_setprio 1
	s_barrier
	v_mfma_f32_16x16x32_bf16 v[126:129], v[154:157], v[186:189], v[126:129]
	v_mfma_f32_16x16x32_bf16 v[122:125], v[162:165], v[186:189], v[122:125]
	v_mfma_f32_16x16x32_bf16 v[118:121], v[154:157], v[194:197], v[118:121]
	v_mfma_f32_16x16x32_bf16 v[110:113], v[162:165], v[194:197], v[110:113]
	v_mfma_f32_16x16x32_bf16 v[102:105], v[154:157], v[202:205], v[102:105]
	v_mfma_f32_16x16x32_bf16 v[94:97], v[162:165], v[202:205], v[94:97]
	v_mfma_f32_16x16x32_bf16 v[86:89], v[154:157], v[210:213], v[86:89]
	v_mfma_f32_16x16x32_bf16 v[78:81], v[162:165], v[210:213], v[78:81]
	v_mfma_f32_16x16x32_bf16 v[126:129], v[158:161], v[190:193], v[126:129]
	v_mfma_f32_16x16x32_bf16 v[122:125], v[166:169], v[190:193], v[122:125]
	v_mfma_f32_16x16x32_bf16 v[118:121], v[158:161], v[198:201], v[118:121]
	v_mfma_f32_16x16x32_bf16 v[110:113], v[166:169], v[198:201], v[110:113]
	v_mfma_f32_16x16x32_bf16 v[102:105], v[158:161], v[206:209], v[102:105]
	v_mfma_f32_16x16x32_bf16 v[94:97], v[166:169], v[206:209], v[94:97]
	v_mfma_f32_16x16x32_bf16 v[86:89], v[158:161], v[214:217], v[86:89]
	v_mfma_f32_16x16x32_bf16 v[78:81], v[166:169], v[214:217], v[78:81]
	s_setprio 0
	s_setprio 1
	v_mfma_f32_16x16x32_bf16 v[114:117], v[170:173], v[186:189], v[114:117]
	v_mfma_f32_16x16x32_bf16 v[106:109], v[178:181], v[186:189], v[106:109]
	v_mfma_f32_16x16x32_bf16 v[98:101], v[170:173], v[194:197], v[98:101]
	v_mfma_f32_16x16x32_bf16 v[90:93], v[178:181], v[194:197], v[90:93]
	v_mfma_f32_16x16x32_bf16 v[82:85], v[170:173], v[202:205], v[82:85]
	v_mfma_f32_16x16x32_bf16 v[74:77], v[178:181], v[202:205], v[74:77]
	v_mfma_f32_16x16x32_bf16 v[70:73], v[170:173], v[210:213], v[70:73]
	v_mfma_f32_16x16x32_bf16 v[66:69], v[178:181], v[210:213], v[66:69]
	v_mfma_f32_16x16x32_bf16 v[114:117], v[174:177], v[190:193], v[114:117]
	v_mfma_f32_16x16x32_bf16 v[106:109], v[182:185], v[190:193], v[106:109]
	v_mfma_f32_16x16x32_bf16 v[98:101], v[174:177], v[198:201], v[98:101]
	v_mfma_f32_16x16x32_bf16 v[90:93], v[182:185], v[198:201], v[90:93]
	v_mfma_f32_16x16x32_bf16 v[82:85], v[174:177], v[206:209], v[82:85]
	v_mfma_f32_16x16x32_bf16 v[74:77], v[182:185], v[206:209], v[74:77]
	v_mfma_f32_16x16x32_bf16 v[70:73], v[174:177], v[214:217], v[70:73]
	v_mfma_f32_16x16x32_bf16 v[66:69], v[182:185], v[214:217], v[66:69]
	s_barrier
	s_setprio 0
	s_add_i32 s30, s60, s38
	v_lshl_add_u64 v[146:147], v[146:147], 0, s[10:11]
	s_mov_b32 m0, s30
	ds_read_b128 v[186:189], v152 offset:49152
	ds_read_b128 v[190:193], v152 offset:50176
	ds_read_b128 v[194:197], v152 offset:51200
	ds_read_b128 v[198:201], v152 offset:52224
	ds_read_b128 v[202:205], v152 offset:53248
	ds_read_b128 v[206:209], v152 offset:54272
	ds_read_b128 v[210:213], v152 offset:55296
	ds_read_b128 v[214:217], v152 offset:56320
	global_load_lds_dwordx4 v[146:147], off
	s_add_i32 m0, s30, 0x2000
	s_add_u32 s28, s28, 0x160080
	v_lshl_add_u64 v[146:147], v[218:219], 0, s[10:11]
	s_addc_u32 s29, s29, 0
	s_add_i32 s30, s61, s38
	global_load_lds_dwordx4 v[146:147], off
	v_lshl_add_u64 v[146:147], s[28:29], 0, v[132:133]
	s_mov_b32 m0, s30
	s_nop 0
	global_load_lds_dwordx4 v[146:147], off
	v_lshl_add_u64 v[146:147], s[28:29], 0, v[136:137]
	s_add_i32 m0, s30, 0x2000
	s_nop 0
	global_load_lds_dwordx4 v[146:147], off
	v_lshl_add_u64 v[146:147], v[220:221], 0, s[10:11]
	s_mov_b32 m0, s44
	s_nop 0
	global_load_lds_dwordx4 v[146:147], off
	v_lshl_add_u64 v[146:147], v[222:223], 0, s[10:11]
	s_mov_b32 m0, s45
	s_nop 0
	global_load_lds_dwordx4 v[146:147], off
	s_waitcnt vmcnt(8)
	s_waitcnt lgkmcnt(0)
	s_setprio 1
	s_barrier
	v_mfma_f32_16x16x32_bf16 v[62:65], v[154:157], v[186:189], v[62:65]
	v_mfma_f32_16x16x32_bf16 v[58:61], v[162:165], v[186:189], v[58:61]
	v_mfma_f32_16x16x32_bf16 v[54:57], v[154:157], v[194:197], v[54:57]
	v_mfma_f32_16x16x32_bf16 v[46:49], v[162:165], v[194:197], v[46:49]
	v_mfma_f32_16x16x32_bf16 v[38:41], v[154:157], v[202:205], v[38:41]
	v_mfma_f32_16x16x32_bf16 v[30:33], v[162:165], v[202:205], v[30:33]
	v_mfma_f32_16x16x32_bf16 v[22:25], v[154:157], v[210:213], v[22:25]
	v_mfma_f32_16x16x32_bf16 v[14:17], v[162:165], v[210:213], v[14:17]
	v_mfma_f32_16x16x32_bf16 v[62:65], v[158:161], v[190:193], v[62:65]
	v_mfma_f32_16x16x32_bf16 v[58:61], v[166:169], v[190:193], v[58:61]
	v_mfma_f32_16x16x32_bf16 v[54:57], v[158:161], v[198:201], v[54:57]
	v_mfma_f32_16x16x32_bf16 v[46:49], v[166:169], v[198:201], v[46:49]
	v_mfma_f32_16x16x32_bf16 v[38:41], v[158:161], v[206:209], v[38:41]
	v_mfma_f32_16x16x32_bf16 v[30:33], v[166:169], v[206:209], v[30:33]
	v_mfma_f32_16x16x32_bf16 v[22:25], v[158:161], v[214:217], v[22:25]
	v_mfma_f32_16x16x32_bf16 v[14:17], v[166:169], v[214:217], v[14:17]
	s_setprio 0
	s_setprio 1
	v_mfma_f32_16x16x32_bf16 v[50:53], v[170:173], v[186:189], v[50:53]
	v_mfma_f32_16x16x32_bf16 v[42:45], v[178:181], v[186:189], v[42:45]
	v_mfma_f32_16x16x32_bf16 v[34:37], v[170:173], v[194:197], v[34:37]
	v_mfma_f32_16x16x32_bf16 v[26:29], v[178:181], v[194:197], v[26:29]
	v_mfma_f32_16x16x32_bf16 v[18:21], v[170:173], v[202:205], v[18:21]
	v_mfma_f32_16x16x32_bf16 v[10:13], v[178:181], v[202:205], v[10:13]
	v_mfma_f32_16x16x32_bf16 v[6:9], v[170:173], v[210:213], v[6:9]
	v_mfma_f32_16x16x32_bf16 v[2:5], v[178:181], v[210:213], v[2:5]
	v_mfma_f32_16x16x32_bf16 v[50:53], v[174:177], v[190:193], v[50:53]
	v_mfma_f32_16x16x32_bf16 v[42:45], v[182:185], v[190:193], v[42:45]
	v_mfma_f32_16x16x32_bf16 v[34:37], v[174:177], v[198:201], v[34:37]
	v_mfma_f32_16x16x32_bf16 v[26:29], v[182:185], v[198:201], v[26:29]
	v_mfma_f32_16x16x32_bf16 v[18:21], v[174:177], v[206:209], v[18:21]
	v_mfma_f32_16x16x32_bf16 v[10:13], v[182:185], v[206:209], v[10:13]
	v_mfma_f32_16x16x32_bf16 v[6:9], v[174:177], v[214:217], v[6:9]
	v_mfma_f32_16x16x32_bf16 v[2:5], v[182:185], v[214:217], v[2:5]
	s_barrier
	s_setprio 0
	s_add_i32 s59, s59, 2
	s_add_u32 s26, s26, 0x100
	s_addc_u32 s27, s27, 0
	s_add_u32 s57, s57, 0x100
	s_addc_u32 s58, s58, 0
	s_cmpk_gt_u32 s59, 0x55

.LBB0_2096:
	s_mov_b32 s100, 0
	s_cmp_lt_i32 s78, 16
	s_cselect_b64 s[4:5], -1, 0
	s_and_b64 s[0:1], s[4:5], s[0:1]
	s_andn2_b64 vcc, exec, s[0:1]
	s_cbranch_vccnz .LBB0_2121
	v_readlane_b32 s4, v254, 14
	s_cmpk_gt_i32 s4, 0x3ff
	v_readfirstlane_b32 s12, v0
	s_cbranch_scc1 .LBB0_2121
	v_readlane_b32 s5, v254, 14
	s_ashr_i32 s33, s5, 31
	s_lshr_b32 s4, s33, 29
	s_add_i32 s7, s5, s4
	s_and_b32 s4, s7, -8
	s_sub_i32 s8, s5, s4
	s_cmp_gt_i32 s8, -1
	s_cbranch_scc0 .LBB0_2100
	s_lshl_b32 s6, s8, 7
	s_cbranch_execz .LBB0_2101
	s_branch .LBB0_2102

.LBB0_2113:
	s_ashr_i32 s25, s24, 31
	s_lshl_b64 s[26:27], s[24:25], 20
	v_readlane_b32 s28, v254, 22
	v_readlane_b32 s29, v254, 23
	s_add_u32 s26, s28, s26
	s_addc_u32 s27, s29, s27
	s_and_b64 s[28:29], s[4:5], exec
	s_cselect_b32 s25, s27, s35
	s_cselect_b32 s57, s26, s34
	s_ashr_i32 s23, s22, 31
	s_lshl_b64 s[28:29], s[22:23], 20
	s_add_u32 s28, s40, s28
	s_addc_u32 s29, s41, s29
	s_and_b64 s[38:39], s[4:5], exec
	s_cselect_b32 s23, s29, s37
	s_cselect_b32 s58, s28, s36
	s_add_u32 s34, s34, 0x80080
	s_addc_u32 s35, s35, 0
	s_add_u32 s59, s36, 0x100
	s_addc_u32 s60, s37, 0
	s_mov_b32 s61, -2
	ds_read_b128 v[154:157], v150
	ds_read_b128 v[158:161], v150 offset:1024
	ds_read_b128 v[162:165], v150 offset:2048
	ds_read_b128 v[166:169], v150 offset:3072
	ds_read_b128 v[170:173], v151
	ds_read_b128 v[174:177], v151 offset:1024
	ds_read_b128 v[178:181], v151 offset:2048
	ds_read_b128 v[182:185], v151 offset:3072
	s_add_u32 s36, s34, 0xfff80080
	s_addc_u32 s37, s35, -1
	s_cmp_eq_u32 s61, 28
	s_cselect_b32 s39, s25, s37
	s_cselect_b32 s38, s57, s36
	s_cselect_b32 s37, s23, s60
	s_cselect_b32 s36, s58, s59
	v_lshl_add_u64 v[146:147], s[34:35], 0, v[138:139]
	s_add_i32 m0, s31, 0xc000
	ds_read_b128 v[186:189], v152
	ds_read_b128 v[190:193], v152 offset:1024
	ds_read_b128 v[194:197], v152 offset:2048
	ds_read_b128 v[198:201], v152 offset:3072
	ds_read_b128 v[202:205], v152 offset:4096
	ds_read_b128 v[206:209], v152 offset:5120
	ds_read_b128 v[210:213], v152 offset:6144
	ds_read_b128 v[214:217], v152 offset:7168
	global_load_lds_dwordx4 v[146:147], off
	v_lshl_add_u64 v[146:147], s[34:35], 0, v[140:141]
	s_add_i32 m0, s31, 0xe000
	s_nop 0
	global_load_lds_dwordx4 v[146:147], off
	s_cmp_lg_u32 s100, 0
	s_cbranch_scc1 .Lrx_2114_0
	s_waitcnt vmcnt(8)
.Lrx_2114_0:
	s_waitcnt vmcnt(24)
	s_waitcnt lgkmcnt(0)
	s_setprio 1
	s_barrier
	v_mfma_f32_16x16x32_bf16 v[126:129], v[154:157], v[186:189], 0
	v_mfma_f32_16x16x32_bf16 v[122:125], v[162:165], v[186:189], 0
	v_mfma_f32_16x16x32_bf16 v[118:121], v[154:157], v[194:197], 0
	v_mfma_f32_16x16x32_bf16 v[110:113], v[162:165], v[194:197], 0
	v_mfma_f32_16x16x32_bf16 v[102:105], v[154:157], v[202:205], 0
	v_mfma_f32_16x16x32_bf16 v[94:97], v[162:165], v[202:205], 0
	v_mfma_f32_16x16x32_bf16 v[86:89], v[154:157], v[210:213], 0
	v_mfma_f32_16x16x32_bf16 v[78:81], v[162:165], v[210:213], 0
	v_mfma_f32_16x16x32_bf16 v[126:129], v[158:161], v[190:193], v[126:129]
	v_mfma_f32_16x16x32_bf16 v[122:125], v[166:169], v[190:193], v[122:125]
	v_mfma_f32_16x16x32_bf16 v[118:121], v[158:161], v[198:201], v[118:121]
	v_mfma_f32_16x16x32_bf16 v[110:113], v[166:169], v[198:201], v[110:113]
	v_mfma_f32_16x16x32_bf16 v[102:105], v[158:161], v[206:209], v[102:105]
	v_mfma_f32_16x16x32_bf16 v[94:97], v[166:169], v[206:209], v[94:97]
	v_mfma_f32_16x16x32_bf16 v[86:89], v[158:161], v[214:217], v[86:89]
	v_mfma_f32_16x16x32_bf16 v[78:81], v[166:169], v[214:217], v[78:81]
	s_setprio 0
	s_setprio 1
	v_mfma_f32_16x16x32_bf16 v[114:117], v[170:173], v[186:189], 0
	v_mfma_f32_16x16x32_bf16 v[106:109], v[178:181], v[186:189], 0
	v_mfma_f32_16x16x32_bf16 v[98:101], v[170:173], v[194:197], 0
	v_mfma_f32_16x16x32_bf16 v[90:93], v[178:181], v[194:197], 0
	v_mfma_f32_16x16x32_bf16 v[82:85], v[170:173], v[202:205], 0
	v_mfma_f32_16x16x32_bf16 v[74:77], v[178:181], v[202:205], 0
	v_mfma_f32_16x16x32_bf16 v[70:73], v[170:173], v[210:213], 0
	v_mfma_f32_16x16x32_bf16 v[66:69], v[178:181], v[210:213], 0
	v_mfma_f32_16x16x32_bf16 v[114:117], v[174:177], v[190:193], v[114:117]
	v_mfma_f32_16x16x32_bf16 v[106:109], v[182:185], v[190:193], v[106:109]
	v_mfma_f32_16x16x32_bf16 v[98:101], v[174:177], v[198:201], v[98:101]
	v_mfma_f32_16x16x32_bf16 v[90:93], v[182:185], v[198:201], v[90:93]
	v_mfma_f32_16x16x32_bf16 v[82:85], v[174:177], v[206:209], v[82:85]
	v_mfma_f32_16x16x32_bf16 v[74:77], v[182:185], v[206:209], v[74:77]
	v_mfma_f32_16x16x32_bf16 v[70:73], v[174:177], v[214:217], v[70:73]
	v_mfma_f32_16x16x32_bf16 v[66:69], v[182:185], v[214:217], v[66:69]
	s_barrier
	s_setprio 0
	s_add_i32 s62, s50, s42
	v_lshl_add_u64 v[146:147], s[36:37], 0, v[132:133]
	s_mov_b32 m0, s62
	ds_read_b128 v[186:189], v152 offset:16384
	ds_read_b128 v[190:193], v152 offset:17408
	ds_read_b128 v[194:197], v152 offset:18432
	ds_read_b128 v[198:201], v152 offset:19456
	ds_read_b128 v[202:205], v152 offset:20480
	ds_read_b128 v[206:209], v152 offset:21504
	ds_read_b128 v[210:213], v152 offset:22528
	ds_read_b128 v[214:217], v152 offset:23552
	global_load_lds_dwordx4 v[146:147], off
	s_add_i32 m0, s62, 0x2000
	s_add_u32 s62, s36, 0x80000
	v_lshl_add_u64 v[218:219], s[36:37], 0, v[136:137]
	s_addc_u32 s63, s37, 0
	s_add_i32 s64, s51, s42
	global_load_lds_dwordx4 v[218:219], off
	v_lshl_add_u64 v[220:221], s[62:63], 0, v[132:133]
	s_mov_b32 m0, s64
	v_lshl_add_u64 v[222:223], s[38:39], 0, v[134:135]
	global_load_lds_dwordx4 v[220:221], off
	v_lshl_add_u64 v[220:221], s[62:63], 0, v[136:137]
	s_add_i32 m0, s64, 0x2000
	s_nop 0
	global_load_lds_dwordx4 v[220:221], off
	v_lshl_add_u64 v[220:221], s[38:39], 0, v[130:131]
	s_mov_b32 m0, s31
	s_nop 0
	global_load_lds_dwordx4 v[220:221], off
	s_mov_b32 m0, s43
	s_nop 0
	global_load_lds_dwordx4 v[222:223], off
	s_cmp_lg_u32 s100, 0
	s_cbranch_scc1 .Lrx_2114_1
	s_waitcnt vmcnt(8)
.Lrx_2114_1:
	s_waitcnt vmcnt(24)
	s_mov_b32 s100, 1
	s_waitcnt lgkmcnt(0)
	s_setprio 1
	s_barrier
	v_mfma_f32_16x16x32_bf16 v[62:65], v[154:157], v[186:189], 0
	v_mfma_f32_16x16x32_bf16 v[58:61], v[162:165], v[186:189], 0
	v_mfma_f32_16x16x32_bf16 v[54:57], v[154:157], v[194:197], 0
	v_mfma_f32_16x16x32_bf16 v[46:49], v[162:165], v[194:197], 0
	v_mfma_f32_16x16x32_bf16 v[38:41], v[154:157], v[202:205], 0
	v_mfma_f32_16x16x32_bf16 v[30:33], v[162:165], v[202:205], 0
	v_mfma_f32_16x16x32_bf16 v[22:25], v[154:157], v[210:213], 0
	v_mfma_f32_16x16x32_bf16 v[14:17], v[162:165], v[210:213], 0
	v_mfma_f32_16x16x32_bf16 v[62:65], v[158:161], v[190:193], v[62:65]
	v_mfma_f32_16x16x32_bf16 v[58:61], v[166:169], v[190:193], v[58:61]
	v_mfma_f32_16x16x32_bf16 v[54:57], v[158:161], v[198:201], v[54:57]
	v_mfma_f32_16x16x32_bf16 v[46:49], v[166:169], v[198:201], v[46:49]
	v_mfma_f32_16x16x32_bf16 v[38:41], v[158:161], v[206:209], v[38:41]
	v_mfma_f32_16x16x32_bf16 v[30:33], v[166:169], v[206:209], v[30:33]
	v_mfma_f32_16x16x32_bf16 v[22:25], v[158:161], v[214:217], v[22:25]
	v_mfma_f32_16x16x32_bf16 v[14:17], v[166:169], v[214:217], v[14:17]
	s_setprio 0
	s_setprio 1
	v_mfma_f32_16x16x32_bf16 v[50:53], v[170:173], v[186:189], 0
	v_mfma_f32_16x16x32_bf16 v[42:45], v[178:181], v[186:189], 0
	v_mfma_f32_16x16x32_bf16 v[34:37], v[170:173], v[194:197], 0
	v_mfma_f32_16x16x32_bf16 v[26:29], v[178:181], v[194:197], 0
	v_mfma_f32_16x16x32_bf16 v[18:21], v[170:173], v[202:205], 0
	v_mfma_f32_16x16x32_bf16 v[10:13], v[178:181], v[202:205], 0
	v_mfma_f32_16x16x32_bf16 v[6:9], v[170:173], v[210:213], 0
	v_mfma_f32_16x16x32_bf16 v[2:5], v[178:181], v[210:213], 0
	v_mfma_f32_16x16x32_bf16 v[50:53], v[174:177], v[190:193], v[50:53]
	v_mfma_f32_16x16x32_bf16 v[42:45], v[182:185], v[190:193], v[42:45]
	v_mfma_f32_16x16x32_bf16 v[34:37], v[174:177], v[198:201], v[34:37]
	v_mfma_f32_16x16x32_bf16 v[26:29], v[182:185], v[198:201], v[26:29]
	v_mfma_f32_16x16x32_bf16 v[18:21], v[174:177], v[206:209], v[18:21]
	v_mfma_f32_16x16x32_bf16 v[10:13], v[182:185], v[206:209], v[10:13]
	v_mfma_f32_16x16x32_bf16 v[6:9], v[174:177], v[214:217], v[6:9]
	v_mfma_f32_16x16x32_bf16 v[2:5], v[182:185], v[214:217], v[2:5]
	s_barrier
	s_setprio 0
	s_add_i32 s62, 0, 0x18000
	v_add_u32_e32 v153, s62, v148
	s_add_i32 s63, 0, 0x1c000
	ds_read_b128 v[154:157], v153
	ds_read_b128 v[158:161], v153 offset:1024
	ds_read_b128 v[162:165], v153 offset:2048
	ds_read_b128 v[166:169], v153 offset:3072
	v_add_u32_e32 v153, s63, v148
	ds_read_b128 v[170:173], v153
	ds_read_b128 v[174:177], v153 offset:1024
	ds_read_b128 v[178:181], v153 offset:2048
	ds_read_b128 v[182:185], v153 offset:3072
	s_add_u32 s38, s38, 0x80000
	s_addc_u32 s39, s39, 0
	s_mov_b32 m0, s44
	v_lshl_add_u64 v[224:225], s[38:39], 0, v[130:131]
	ds_read_b128 v[186:189], v152 offset:32768
	ds_read_b128 v[190:193], v152 offset:33792
	ds_read_b128 v[194:197], v152 offset:34816
	ds_read_b128 v[198:201], v152 offset:35840
	ds_read_b128 v[202:205], v152 offset:36864
	ds_read_b128 v[206:209], v152 offset:37888
	ds_read_b128 v[210:213], v152 offset:38912
	ds_read_b128 v[214:217], v152 offset:39936
	global_load_lds_dwordx4 v[224:225], off
	v_lshl_add_u64 v[224:225], s[38:39], 0, v[134:135]
	s_mov_b32 m0, s45
	s_nop 0
	global_load_lds_dwordx4 v[224:225], off
	s_waitcnt vmcnt(8)
	s_waitcnt lgkmcnt(0)
	s_setprio 1
	s_barrier
	v_mfma_f32_16x16x32_bf16 v[126:129], v[154:157], v[186:189], v[126:129]
	v_mfma_f32_16x16x32_bf16 v[122:125], v[162:165], v[186:189], v[122:125]
	v_mfma_f32_16x16x32_bf16 v[118:121], v[154:157], v[194:197], v[118:121]
	v_mfma_f32_16x16x32_bf16 v[110:113], v[162:165], v[194:197], v[110:113]
	v_mfma_f32_16x16x32_bf16 v[102:105], v[154:157], v[202:205], v[102:105]
	v_mfma_f32_16x16x32_bf16 v[94:97], v[162:165], v[202:205], v[94:97]
	v_mfma_f32_16x16x32_bf16 v[86:89], v[154:157], v[210:213], v[86:89]
	v_mfma_f32_16x16x32_bf16 v[78:81], v[162:165], v[210:213], v[78:81]
	v_mfma_f32_16x16x32_bf16 v[126:129], v[158:161], v[190:193], v[126:129]
	v_mfma_f32_16x16x32_bf16 v[122:125], v[166:169], v[190:193], v[122:125]
	v_mfma_f32_16x16x32_bf16 v[118:121], v[158:161], v[198:201], v[118:121]
	v_mfma_f32_16x16x32_bf16 v[110:113], v[166:169], v[198:201], v[110:113]
	v_mfma_f32_16x16x32_bf16 v[102:105], v[158:161], v[206:209], v[102:105]
	v_mfma_f32_16x16x32_bf16 v[94:97], v[166:169], v[206:209], v[94:97]
	v_mfma_f32_16x16x32_bf16 v[86:89], v[158:161], v[214:217], v[86:89]
	v_mfma_f32_16x16x32_bf16 v[78:81], v[166:169], v[214:217], v[78:81]
	s_setprio 0
	s_setprio 1
	v_mfma_f32_16x16x32_bf16 v[114:117], v[170:173], v[186:189], v[114:117]
	v_mfma_f32_16x16x32_bf16 v[106:109], v[178:181], v[186:189], v[106:109]
	v_mfma_f32_16x16x32_bf16 v[98:101], v[170:173], v[194:197], v[98:101]
	v_mfma_f32_16x16x32_bf16 v[90:93], v[178:181], v[194:197], v[90:93]
	v_mfma_f32_16x16x32_bf16 v[82:85], v[170:173], v[202:205], v[82:85]
	v_mfma_f32_16x16x32_bf16 v[74:77], v[178:181], v[202:205], v[74:77]
	v_mfma_f32_16x16x32_bf16 v[70:73], v[170:173], v[210:213], v[70:73]
	v_mfma_f32_16x16x32_bf16 v[66:69], v[178:181], v[210:213], v[66:69]
	v_mfma_f32_16x16x32_bf16 v[114:117], v[174:177], v[190:193], v[114:117]
	v_mfma_f32_16x16x32_bf16 v[106:109], v[182:185], v[190:193], v[106:109]
	v_mfma_f32_16x16x32_bf16 v[98:101], v[174:177], v[198:201], v[98:101]
	v_mfma_f32_16x16x32_bf16 v[90:93], v[182:185], v[198:201], v[90:93]
	v_mfma_f32_16x16x32_bf16 v[82:85], v[174:177], v[206:209], v[82:85]
	v_mfma_f32_16x16x32_bf16 v[74:77], v[182:185], v[206:209], v[74:77]
	v_mfma_f32_16x16x32_bf16 v[70:73], v[174:177], v[214:217], v[70:73]
	v_mfma_f32_16x16x32_bf16 v[66:69], v[182:185], v[214:217], v[66:69]
	s_barrier
	s_setprio 0
	s_add_i32 s38, s62, s42
	v_lshl_add_u64 v[146:147], v[146:147], 0, s[10:11]
	s_mov_b32 m0, s38
	ds_read_b128 v[186:189], v152 offset:49152
	ds_read_b128 v[190:193], v152 offset:50176
	ds_read_b128 v[194:197], v152 offset:51200
	ds_read_b128 v[198:201], v152 offset:52224
	ds_read_b128 v[202:205], v152 offset:53248
	ds_read_b128 v[206:209], v152 offset:54272
	ds_read_b128 v[210:213], v152 offset:55296
	ds_read_b128 v[214:217], v152 offset:56320
	global_load_lds_dwordx4 v[146:147], off
	s_add_i32 m0, s38, 0x2000
	s_add_u32 s36, s36, 0x80080
	v_lshl_add_u64 v[146:147], v[218:219], 0, s[10:11]
	s_addc_u32 s37, s37, 0
	s_add_i32 s38, s63, s42
	global_load_lds_dwordx4 v[146:147], off
	v_lshl_add_u64 v[146:147], s[36:37], 0, v[132:133]
	s_mov_b32 m0, s38
	s_nop 0
	global_load_lds_dwordx4 v[146:147], off
	v_lshl_add_u64 v[146:147], s[36:37], 0, v[136:137]
	s_add_i32 m0, s38, 0x2000
	s_nop 0
	global_load_lds_dwordx4 v[146:147], off
	v_lshl_add_u64 v[146:147], v[220:221], 0, s[10:11]
	s_mov_b32 m0, s47
	s_nop 0
	global_load_lds_dwordx4 v[146:147], off
	v_lshl_add_u64 v[146:147], v[222:223], 0, s[10:11]
	s_mov_b32 m0, s48
	s_nop 0
	global_load_lds_dwordx4 v[146:147], off
	s_waitcnt vmcnt(8)
	s_waitcnt lgkmcnt(0)
	s_setprio 1
	s_barrier
	v_mfma_f32_16x16x32_bf16 v[62:65], v[154:157], v[186:189], v[62:65]
	v_mfma_f32_16x16x32_bf16 v[58:61], v[162:165], v[186:189], v[58:61]
	v_mfma_f32_16x16x32_bf16 v[54:57], v[154:157], v[194:197], v[54:57]
	v_mfma_f32_16x16x32_bf16 v[46:49], v[162:165], v[194:197], v[46:49]
	v_mfma_f32_16x16x32_bf16 v[38:41], v[154:157], v[202:205], v[38:41]
	v_mfma_f32_16x16x32_bf16 v[30:33], v[162:165], v[202:205], v[30:33]
	v_mfma_f32_16x16x32_bf16 v[22:25], v[154:157], v[210:213], v[22:25]
	v_mfma_f32_16x16x32_bf16 v[14:17], v[162:165], v[210:213], v[14:17]
	v_mfma_f32_16x16x32_bf16 v[62:65], v[158:161], v[190:193], v[62:65]
	v_mfma_f32_16x16x32_bf16 v[58:61], v[166:169], v[190:193], v[58:61]
	v_mfma_f32_16x16x32_bf16 v[54:57], v[158:161], v[198:201], v[54:57]
	v_mfma_f32_16x16x32_bf16 v[46:49], v[166:169], v[198:201], v[46:49]
	v_mfma_f32_16x16x32_bf16 v[38:41], v[158:161], v[206:209], v[38:41]
	v_mfma_f32_16x16x32_bf16 v[30:33], v[166:169], v[206:209], v[30:33]
	v_mfma_f32_16x16x32_bf16 v[22:25], v[158:161], v[214:217], v[22:25]
	v_mfma_f32_16x16x32_bf16 v[14:17], v[166:169], v[214:217], v[14:17]
	s_setprio 0
	s_setprio 1
	v_mfma_f32_16x16x32_bf16 v[50:53], v[170:173], v[186:189], v[50:53]
	v_mfma_f32_16x16x32_bf16 v[42:45], v[178:181], v[186:189], v[42:45]
	v_mfma_f32_16x16x32_bf16 v[34:37], v[170:173], v[194:197], v[34:37]
	v_mfma_f32_16x16x32_bf16 v[26:29], v[178:181], v[194:197], v[26:29]
	v_mfma_f32_16x16x32_bf16 v[18:21], v[170:173], v[202:205], v[18:21]
	v_mfma_f32_16x16x32_bf16 v[10:13], v[178:181], v[202:205], v[10:13]
	v_mfma_f32_16x16x32_bf16 v[6:9], v[170:173], v[210:213], v[6:9]
	v_mfma_f32_16x16x32_bf16 v[2:5], v[178:181], v[210:213], v[2:5]
	v_mfma_f32_16x16x32_bf16 v[50:53], v[174:177], v[190:193], v[50:53]
	v_mfma_f32_16x16x32_bf16 v[42:45], v[182:185], v[190:193], v[42:45]
	v_mfma_f32_16x16x32_bf16 v[34:37], v[174:177], v[198:201], v[34:37]
	v_mfma_f32_16x16x32_bf16 v[26:29], v[182:185], v[198:201], v[26:29]
	v_mfma_f32_16x16x32_bf16 v[18:21], v[174:177], v[206:209], v[18:21]
	v_mfma_f32_16x16x32_bf16 v[10:13], v[182:185], v[206:209], v[10:13]
	v_mfma_f32_16x16x32_bf16 v[6:9], v[174:177], v[214:217], v[6:9]
	v_mfma_f32_16x16x32_bf16 v[2:5], v[182:185], v[214:217], v[2:5]
	s_barrier
	s_setprio 0
	s_add_i32 s61, s61, 2
	s_add_u32 s34, s34, 0x100
	s_addc_u32 s35, s35, 0
	s_add_u32 s59, s59, 0x100
	s_addc_u32 s60, s60, 0
	s_cmp_gt_u32 s61, 29

.LBB0_2356:
	s_mov_b32 s100, 0
	s_cmp_lt_i32 s78, 19
	s_cselect_b64 s[2:3], -1, 0
	s_min_u32 s58, s50, 0x108
	s_and_b64 s[2:3], s[2:3], s[0:1]
	s_cmp_gt_i32 s50, 0
	s_cselect_b64 s[0:1], -1, 0
	s_and_b64 s[4:5], s[2:3], s[0:1]
	s_andn2_b64 vcc, exec, s[4:5]
	s_mov_b32 s74, s66
	s_cbranch_vccnz .LBB0_2373
	s_mul_i32 s6, s58, 56
	v_readlane_b32 s4, v254, 14
	s_cmp_ge_i32 s4, s6
	v_readfirstlane_b32 s4, v0
	s_cbranch_scc1 .LBB0_2373
	v_lshrrev_b32_e32 v1, 5, v0
	v_lshrrev_b32_e32 v3, 1, v0
	v_and_b32_e32 v1, 4, v1
	v_bfe_u32 v2, v0, 2, 2
	s_waitcnt lgkmcnt(0)
	v_and_b32_e32 v13, 24, v3
	s_add_u32 s19, s86, 0x25800000
	v_or3_b32 v1, v1, v2, v13
	v_lshlrev_b32_e32 v2, 4, v0
	s_addc_u32 s40, s87, 0
	v_or_b32_e32 v10, 0x2000, v2
	s_add_u32 s41, s86, 0x8800000
	v_lshrrev_b32_e32 v3, 7, v10
	s_movk_i32 s7, 0x60
	v_readlane_b32 s9, v254, 14
	s_addc_u32 s42, s87, 0
	v_and_or_b32 v4, v3, s7, v1
	v_bfe_u32 v14, v0, 2, 4
	s_movk_i32 s7, 0x70
	s_ashr_i32 s45, s9, 31
	v_and_or_b32 v3, v3, s7, v14
	s_lshr_b32 s7, s45, 29
	s_add_i32 s7, s9, s7
	s_lshr_b32 s12, s4, 6
	s_mul_i32 s44, s58, 7
	s_ashr_i32 s8, s7, 3
	s_and_b32 s7, s7, -8
	s_lshr_b32 s5, s4, 8
	s_lshl_b32 s43, s12, 10
	s_sub_i32 s7, s9, s7
	s_add_i32 s46, s44, 1
	s_cmp_lt_i32 s7, 0
	s_cselect_b32 s9, s46, s44
	s_mul_i32 s7, s9, s7
	s_add_i32 s7, s7, s8
	s_mul_hi_i32 s8, s7, 0x92492493
	s_add_i32 s8, s8, s7
	s_lshr_b32 s9, s8, 31
	s_ashr_i32 s8, s8, 8
	s_add_i32 s8, s8, s9
	s_lshl_b32 s9, s8, 3
	v_and_b32_e32 v5, 32, v0
	s_sub_i32 s10, s58, s9
	v_bitop3_b32 v11, v2, v5, 48 bitop3:0x6c
	v_and_b32_e32 v12, 64, v0
	s_min_i32 s10, s10, 8
	v_or_b32_e32 v2, v11, v12
	s_abs_i32 s11, s10
	s_waitcnt vmcnt(0)
	v_lshl_or_b32 v162, v4, 11, v2
	v_cvt_f32_u32_e32 v4, s11
	v_lshl_or_b32 v164, v3, 11, v2
	v_lshrrev_b32_e32 v3, 3, v0
	v_and_or_b32 v1, v3, 32, v1
	v_lshl_or_b32 v166, v1, 11, v2
	v_and_or_b32 v1, v3, 48, v14
	v_lshl_or_b32 v168, v1, 11, v2
	v_rcp_iflag_f32_e32 v1, v4
	s_sub_i32 s16, 0, s11
	s_mulk_i32 s8, 0x1c0
	s_sub_i32 s7, s7, s8
	v_mul_f32_e32 v1, 0x4f7ffffe, v1
	v_cvt_u32_f32_e32 v1, v1
	s_abs_i32 s13, s7
	s_xor_b32 s8, s7, s10
	s_ashr_i32 s8, s8, 31
	v_readfirstlane_b32 s17, v1
	s_mul_i32 s16, s16, s17
	s_mul_hi_u32 s16, s17, s16
	s_add_i32 s17, s17, s16
	s_mul_hi_u32 s16, s13, s17
	s_mul_i32 s17, s16, s11
	s_sub_i32 s13, s13, s17
	s_add_i32 s17, s16, 1
	s_sub_i32 s18, s13, s11
	s_cmp_ge_u32 s13, s11
	s_cselect_b32 s16, s17, s16
	s_cselect_b32 s13, s18, s13
	s_add_i32 s17, s16, 1
	s_cmp_ge_u32 s13, s11
	s_cselect_b32 s11, s17, s16
	s_xor_b32 s11, s11, s8
	s_sub_i32 s65, s11, s8
	s_mul_i32 s8, s65, s10
	s_sub_i32 s7, s7, s8
	s_add_i32 s30, s9, s7
	s_cmp_ge_i32 s30, s33
	s_cselect_b64 s[8:9], -1, 0
	s_cmp_ge_i32 s30, s57
	v_cndmask_b32_e64 v1, 0, 1, s[8:9]
	s_cselect_b64 s[8:9], -1, 0
	s_cmp_ge_i32 s30, s52
	v_cndmask_b32_e64 v2, 0, 1, s[8:9]
	s_cselect_b64 s[8:9], -1, 0
	v_readfirstlane_b32 s7, v1
	v_readfirstlane_b32 s10, v2
	s_cmp_lg_u64 s[8:9], 0
	s_addc_u32 s7, s7, s10
	s_cmp_ge_i32 s30, s53
	s_cselect_b64 s[8:9], -1, 0
	s_cmp_ge_i32 s30, s54
	v_cndmask_b32_e64 v1, 0, 1, s[8:9]
	s_cselect_b64 s[8:9], -1, 0
	v_readfirstlane_b32 s10, v1
	s_cmp_lg_u64 s[8:9], 0
	s_addc_u32 s7, s7, s10
	s_cmp_ge_i32 s30, s55
	s_cselect_b64 s[8:9], -1, 0
	s_cmp_ge_i32 s30, s56
	v_cndmask_b32_e64 v1, 0, 1, s[8:9]
	s_cselect_b64 s[8:9], -1, 0
	v_readfirstlane_b32 s10, v1
	s_cmp_lg_u64 s[8:9], 0
	s_addc_u32 s7, s7, s10
	s_mul_i32 s7, s7, 56
	s_add_i32 s8, s7, s65
	s_ashr_i32 s9, s8, 31
	s_ashr_i32 s31, s30, 31
	s_lshl_b64 s[8:9], s[8:9], 19
	s_lshl_b64 s[10:11], s[30:31], 19
	s_add_u32 s36, s41, s8
	s_addc_u32 s37, s42, s9
	s_add_i32 s31, s43, 0
	s_add_i32 m0, s31, 0x10000
	v_mov_b32_e32 v167, 0
	global_load_lds_dwordx4 v166, s[36:37]
	s_add_i32 m0, s31, 0x12000
	s_add_u32 s8, s36, 0x40000
	global_load_lds_dwordx4 v162, s[36:37]
	s_addc_u32 s9, s37, 0
	s_add_i32 m0, s31, 0x14000
	v_mov_b32_e32 v163, v167
	global_load_lds_dwordx4 v166, s[8:9]
	s_add_i32 m0, s31, 0x16000
	s_add_u32 s34, s19, s10
	s_addc_u32 s35, s40, s11
	s_add_i32 s47, s31, 0x2000
	global_load_lds_dwordx4 v162, s[8:9]
	s_mov_b32 m0, s31
	s_add_u32 s8, s34, 0x40000
	global_load_lds_dwordx4 v168, s[34:35]
	s_mov_b32 m0, s47
	s_addc_u32 s9, s35, 0
	s_add_i32 s48, s31, 0x4000
	global_load_lds_dwordx4 v164, s[34:35]
	s_mov_b32 m0, s48
	s_add_i32 s49, s31, 0x6000
	global_load_lds_dwordx4 v168, s[8:9]
	s_mov_b32 m0, s49
	v_mov_b32_e32 v169, v167
	global_load_lds_dwordx4 v164, s[8:9]
	v_mov_b32_e32 v165, v167
	s_cmp_eq_u32 s5, 1
	s_mov_b32 s7, 0
	v_lshl_add_u64 v[8:9], s[36:37], 0, v[166:167]
	v_lshl_add_u64 v[6:7], s[36:37], 0, v[162:163]
	v_lshl_add_u64 v[2:3], s[34:35], 0, v[168:169]
	s_cselect_b64 s[8:9], -1, 0
	s_cmp_lg_u32 s5, 1
	v_lshl_add_u64 v[4:5], s[34:35], 0, v[164:165]
	s_cbranch_scc1 .LBB0_2360
	s_barrier

.LBB0_2365:
	s_ashr_i32 s23, s22, 31
	s_lshl_b64 s[26:27], s[22:23], 19
	s_add_u32 s26, s19, s26
	s_addc_u32 s27, s40, s27
	s_and_b64 s[28:29], s[4:5], exec
	s_cselect_b32 s23, s27, s35
	s_cselect_b32 s66, s26, s34
	s_ashr_i32 s25, s24, 31
	s_lshl_b64 s[28:29], s[24:25], 19
	s_add_u32 s28, s41, s28
	s_addc_u32 s29, s42, s29
	s_and_b64 s[38:39], s[4:5], exec
	s_cselect_b32 s25, s29, s37
	s_cselect_b32 s67, s28, s36
	s_add_u32 s34, s34, 0x40080
	s_addc_u32 s35, s35, 0
	s_add_u32 s68, s36, 0x100
	s_addc_u32 s69, s37, 0
	s_mov_b32 s70, -2
	ds_read_b128 v[18:21], v186
	ds_read_b128 v[22:25], v186 offset:1024
	ds_read_b128 v[26:29], v186 offset:2048
	ds_read_b128 v[30:33], v186 offset:3072
	ds_read_b128 v[2:5], v187
	ds_read_b128 v[6:9], v187 offset:1024
	ds_read_b128 v[10:13], v187 offset:2048
	ds_read_b128 v[14:17], v187 offset:3072
	s_add_u32 s36, s34, 0xfffc0080
	s_addc_u32 s37, s35, -1
	s_cmp_eq_u32 s70, 12
	s_cselect_b32 s39, s23, s37
	s_cselect_b32 s38, s66, s36
	s_cselect_b32 s37, s25, s69
	s_cselect_b32 s36, s67, s68
	v_lshl_add_u64 v[208:209], s[34:35], 0, v[170:171]
	s_add_i32 m0, s31, 0xc000
	ds_read_b128 v[176:179], v188
	ds_read_b128 v[180:183], v188 offset:1024
	ds_read_b128 v[192:195], v188 offset:2048
	ds_read_b128 v[196:199], v188 offset:3072
	ds_read_b128 v[200:203], v188 offset:4096
	ds_read_b128 v[204:207], v188 offset:5120
	ds_read_b128 v[216:219], v188 offset:6144
	ds_read_b128 v[220:223], v188 offset:7168
	global_load_lds_dwordx4 v[208:209], off
	v_lshl_add_u64 v[208:209], s[34:35], 0, v[172:173]
	s_add_i32 m0, s31, 0xe000
	s_nop 0
	global_load_lds_dwordx4 v[208:209], off
	s_cmp_lg_u32 s100, 0
	s_cbranch_scc1 .Lrx_2366_0
	s_waitcnt vmcnt(8)
.Lrx_2366_0:
	s_waitcnt vmcnt(16)
	s_waitcnt lgkmcnt(0)
	s_setprio 1
	s_barrier
	v_mfma_scale_f32_16x16x128_f8f6f4 v[158:161], v[18:25], v[176:183], 0, v189, v190 op_sel_hi:[0,0,0]
	v_mfma_scale_f32_16x16x128_f8f6f4 v[150:153], v[26:33], v[176:183], 0, v189, v190 op_sel_hi:[0,0,0]
	v_mfma_scale_f32_16x16x128_f8f6f4 v[142:145], v[18:25], v[192:199], 0, v189, v190 op_sel_hi:[0,0,0]
	v_mfma_scale_f32_16x16x128_f8f6f4 v[134:137], v[26:33], v[192:199], 0, v189, v190 op_sel_hi:[0,0,0]
	v_mfma_scale_f32_16x16x128_f8f6f4 v[126:129], v[18:25], v[200:207], 0, v189, v190 op_sel_hi:[0,0,0]
	v_mfma_scale_f32_16x16x128_f8f6f4 v[118:121], v[26:33], v[200:207], 0, v189, v190 op_sel_hi:[0,0,0]
	v_mfma_scale_f32_16x16x128_f8f6f4 v[110:113], v[18:25], v[216:223], 0, v189, v190 op_sel_hi:[0,0,0]
	v_mfma_scale_f32_16x16x128_f8f6f4 v[102:105], v[26:33], v[216:223], 0, v189, v190 op_sel_hi:[0,0,0]
	s_setprio 0
	s_setprio 1
	v_mfma_scale_f32_16x16x128_f8f6f4 v[154:157], v[2:9], v[176:183], 0, v189, v190 op_sel_hi:[0,0,0]
	v_mfma_scale_f32_16x16x128_f8f6f4 v[146:149], v[10:17], v[176:183], 0, v189, v190 op_sel_hi:[0,0,0]
	v_mfma_scale_f32_16x16x128_f8f6f4 v[138:141], v[2:9], v[192:199], 0, v189, v190 op_sel_hi:[0,0,0]
	v_mfma_scale_f32_16x16x128_f8f6f4 v[130:133], v[10:17], v[192:199], 0, v189, v190 op_sel_hi:[0,0,0]
	v_mfma_scale_f32_16x16x128_f8f6f4 v[122:125], v[2:9], v[200:207], 0, v189, v190 op_sel_hi:[0,0,0]
	v_mfma_scale_f32_16x16x128_f8f6f4 v[114:117], v[10:17], v[200:207], 0, v189, v190 op_sel_hi:[0,0,0]
	v_mfma_scale_f32_16x16x128_f8f6f4 v[106:109], v[2:9], v[216:223], 0, v189, v190 op_sel_hi:[0,0,0]
	v_mfma_scale_f32_16x16x128_f8f6f4 v[98:101], v[10:17], v[216:223], 0, v189, v190 op_sel_hi:[0,0,0]
	s_barrier
	s_setprio 0
	s_add_i32 s71, s60, s43
	v_lshl_add_u64 v[176:177], s[36:37], 0, v[166:167]
	s_mov_b32 m0, s71
	ds_read_b128 v[192:195], v188 offset:16384
	ds_read_b128 v[196:199], v188 offset:17408
	ds_read_b128 v[200:203], v188 offset:18432
	ds_read_b128 v[204:207], v188 offset:19456
	ds_read_b128 v[216:219], v188 offset:20480
	ds_read_b128 v[220:223], v188 offset:21504
	ds_read_b128 v[224:227], v188 offset:22528
	ds_read_b128 v[228:231], v188 offset:23552
	global_load_lds_dwordx4 v[176:177], off
	s_add_i32 m0, s71, 0x2000
	s_add_u32 s72, s36, 0x40000
	v_lshl_add_u64 v[178:179], s[36:37], 0, v[162:163]
	s_addc_u32 s73, s37, 0
	s_add_i32 s71, s61, s43
	global_load_lds_dwordx4 v[178:179], off
	v_lshl_add_u64 v[180:181], s[72:73], 0, v[166:167]
	s_mov_b32 m0, s71
	v_lshl_add_u64 v[182:183], s[38:39], 0, v[164:165]
	global_load_lds_dwordx4 v[180:181], off
	v_lshl_add_u64 v[180:181], s[72:73], 0, v[162:163]
	s_add_i32 m0, s71, 0x2000
	s_nop 0
	global_load_lds_dwordx4 v[180:181], off
	v_lshl_add_u64 v[180:181], s[38:39], 0, v[168:169]
	s_mov_b32 m0, s31
	s_nop 0
	global_load_lds_dwordx4 v[180:181], off
	s_mov_b32 m0, s47
	s_nop 0
	global_load_lds_dwordx4 v[182:183], off
	s_cmp_lg_u32 s100, 0
	s_cbranch_scc1 .Lrx_2366_1
	s_waitcnt vmcnt(8)
.Lrx_2366_1:
	s_waitcnt vmcnt(16)
	s_mov_b32 s100, 1
	s_waitcnt lgkmcnt(0)
	s_setprio 1
	s_barrier
	v_mfma_scale_f32_16x16x128_f8f6f4 v[94:97], v[18:25], v[192:199], 0, v189, v190 op_sel_hi:[0,0,0]
	v_mfma_scale_f32_16x16x128_f8f6f4 v[86:89], v[26:33], v[192:199], 0, v189, v190 op_sel_hi:[0,0,0]
	v_mfma_scale_f32_16x16x128_f8f6f4 v[78:81], v[18:25], v[200:207], 0, v189, v190 op_sel_hi:[0,0,0]
	v_mfma_scale_f32_16x16x128_f8f6f4 v[70:73], v[26:33], v[200:207], 0, v189, v190 op_sel_hi:[0,0,0]
	v_mfma_scale_f32_16x16x128_f8f6f4 v[62:65], v[18:25], v[216:223], 0, v189, v190 op_sel_hi:[0,0,0]
	v_mfma_scale_f32_16x16x128_f8f6f4 v[54:57], v[26:33], v[216:223], 0, v189, v190 op_sel_hi:[0,0,0]
	v_mfma_scale_f32_16x16x128_f8f6f4 v[46:49], v[18:25], v[224:231], 0, v189, v190 op_sel_hi:[0,0,0]
	v_mfma_scale_f32_16x16x128_f8f6f4 v[38:41], v[26:33], v[224:231], 0, v189, v190 op_sel_hi:[0,0,0]
	s_setprio 0
	s_setprio 1
	v_mfma_scale_f32_16x16x128_f8f6f4 v[90:93], v[2:9], v[192:199], 0, v189, v190 op_sel_hi:[0,0,0]
	v_mfma_scale_f32_16x16x128_f8f6f4 v[82:85], v[10:17], v[192:199], 0, v189, v190 op_sel_hi:[0,0,0]
	v_mfma_scale_f32_16x16x128_f8f6f4 v[74:77], v[2:9], v[200:207], 0, v189, v190 op_sel_hi:[0,0,0]
	v_mfma_scale_f32_16x16x128_f8f6f4 v[66:69], v[10:17], v[200:207], 0, v189, v190 op_sel_hi:[0,0,0]
	v_mfma_scale_f32_16x16x128_f8f6f4 v[58:61], v[2:9], v[216:223], 0, v189, v190 op_sel_hi:[0,0,0]
	v_mfma_scale_f32_16x16x128_f8f6f4 v[50:53], v[10:17], v[216:223], 0, v189, v190 op_sel_hi:[0,0,0]
	v_mfma_scale_f32_16x16x128_f8f6f4 v[42:45], v[2:9], v[224:231], 0, v189, v190 op_sel_hi:[0,0,0]
	v_mfma_scale_f32_16x16x128_f8f6f4 v[34:37], v[10:17], v[224:231], 0, v189, v190 op_sel_hi:[0,0,0]
	s_barrier
	s_setprio 0
	s_add_i32 s71, 0, 0x18000
	s_add_i32 s72, 0, 0x1c000
	v_add_u32_e32 v14, s71, v184
	v_add_u32_e32 v30, s72, v184
	ds_read_b128 v[2:5], v14
	ds_read_b128 v[6:9], v14 offset:1024
	ds_read_b128 v[10:13], v14 offset:2048
	ds_read_b128 v[14:17], v14 offset:3072
	ds_read_b128 v[18:21], v30
	ds_read_b128 v[22:25], v30 offset:1024
	ds_read_b128 v[26:29], v30 offset:2048
	ds_read_b128 v[30:33], v30 offset:3072
	s_add_u32 s38, s38, 0x40000
	s_addc_u32 s39, s39, 0
	s_mov_b32 m0, s48
	v_lshl_add_u64 v[208:209], s[38:39], 0, v[168:169]
	ds_read_b128 v[192:195], v188 offset:32768
	ds_read_b128 v[196:199], v188 offset:33792
	ds_read_b128 v[200:203], v188 offset:34816
	ds_read_b128 v[204:207], v188 offset:35840
	ds_read_b128 v[216:219], v188 offset:36864
	ds_read_b128 v[220:223], v188 offset:37888
	ds_read_b128 v[224:227], v188 offset:38912
	ds_read_b128 v[228:231], v188 offset:39936
	global_load_lds_dwordx4 v[208:209], off
	v_lshl_add_u64 v[208:209], s[38:39], 0, v[164:165]
	s_mov_b32 m0, s49
	s_nop 0
	global_load_lds_dwordx4 v[208:209], off
	s_waitcnt vmcnt(8)
	s_waitcnt lgkmcnt(0)
	s_setprio 1
	s_barrier
	v_mfma_scale_f32_16x16x128_f8f6f4 v[158:161], v[2:9], v[192:199], v[158:161], v189, v190 op_sel_hi:[0,0,0]
	v_mfma_scale_f32_16x16x128_f8f6f4 v[150:153], v[10:17], v[192:199], v[150:153], v189, v190 op_sel_hi:[0,0,0]
	v_mfma_scale_f32_16x16x128_f8f6f4 v[142:145], v[2:9], v[200:207], v[142:145], v189, v190 op_sel_hi:[0,0,0]
	v_mfma_scale_f32_16x16x128_f8f6f4 v[134:137], v[10:17], v[200:207], v[134:137], v189, v190 op_sel_hi:[0,0,0]
	v_mfma_scale_f32_16x16x128_f8f6f4 v[126:129], v[2:9], v[216:223], v[126:129], v189, v190 op_sel_hi:[0,0,0]
	v_mfma_scale_f32_16x16x128_f8f6f4 v[118:121], v[10:17], v[216:223], v[118:121], v189, v190 op_sel_hi:[0,0,0]
	v_mfma_scale_f32_16x16x128_f8f6f4 v[110:113], v[2:9], v[224:231], v[110:113], v189, v190 op_sel_hi:[0,0,0]
	v_mfma_scale_f32_16x16x128_f8f6f4 v[102:105], v[10:17], v[224:231], v[102:105], v189, v190 op_sel_hi:[0,0,0]
	s_setprio 0
	s_setprio 1
	v_mfma_scale_f32_16x16x128_f8f6f4 v[154:157], v[18:25], v[192:199], v[154:157], v189, v190 op_sel_hi:[0,0,0]
	v_mfma_scale_f32_16x16x128_f8f6f4 v[146:149], v[26:33], v[192:199], v[146:149], v189, v190 op_sel_hi:[0,0,0]
	v_mfma_scale_f32_16x16x128_f8f6f4 v[138:141], v[18:25], v[200:207], v[138:141], v189, v190 op_sel_hi:[0,0,0]
	v_mfma_scale_f32_16x16x128_f8f6f4 v[130:133], v[26:33], v[200:207], v[130:133], v189, v190 op_sel_hi:[0,0,0]
	v_mfma_scale_f32_16x16x128_f8f6f4 v[122:125], v[18:25], v[216:223], v[122:125], v189, v190 op_sel_hi:[0,0,0]
	v_mfma_scale_f32_16x16x128_f8f6f4 v[114:117], v[26:33], v[216:223], v[114:117], v189, v190 op_sel_hi:[0,0,0]
	v_mfma_scale_f32_16x16x128_f8f6f4 v[106:109], v[18:25], v[224:231], v[106:109], v189, v190 op_sel_hi:[0,0,0]
	v_mfma_scale_f32_16x16x128_f8f6f4 v[98:101], v[26:33], v[224:231], v[98:101], v189, v190 op_sel_hi:[0,0,0]
	s_barrier
	s_setprio 0
	s_add_i32 s38, s71, s43
	v_lshl_add_u64 v[176:177], v[176:177], 0, s[12:13]
	s_mov_b32 m0, s38
	ds_read_b128 v[192:195], v188 offset:49152
	ds_read_b128 v[196:199], v188 offset:50176
	ds_read_b128 v[200:203], v188 offset:51200
	ds_read_b128 v[204:207], v188 offset:52224
	ds_read_b128 v[216:219], v188 offset:53248
	ds_read_b128 v[220:223], v188 offset:54272
	ds_read_b128 v[224:227], v188 offset:55296
	ds_read_b128 v[228:231], v188 offset:56320
	global_load_lds_dwordx4 v[176:177], off
	s_add_i32 m0, s38, 0x2000
	s_add_u32 s36, s36, 0x40080
	v_lshl_add_u64 v[176:177], v[178:179], 0, s[12:13]
	s_addc_u32 s37, s37, 0
	s_add_i32 s38, s72, s43
	global_load_lds_dwordx4 v[176:177], off
	v_lshl_add_u64 v[176:177], s[36:37], 0, v[166:167]
	s_mov_b32 m0, s38
	s_nop 0
	global_load_lds_dwordx4 v[176:177], off
	v_lshl_add_u64 v[176:177], s[36:37], 0, v[162:163]
	s_add_i32 m0, s38, 0x2000
	s_nop 0
	global_load_lds_dwordx4 v[176:177], off
	v_lshl_add_u64 v[176:177], v[180:181], 0, s[12:13]
	s_mov_b32 m0, s50
	s_nop 0
	global_load_lds_dwordx4 v[176:177], off
	v_lshl_add_u64 v[176:177], v[182:183], 0, s[12:13]
	s_mov_b32 m0, s51
	s_nop 0
	global_load_lds_dwordx4 v[176:177], off
	s_waitcnt vmcnt(8)
	s_waitcnt lgkmcnt(0)
	s_setprio 1
	s_barrier
	v_mfma_scale_f32_16x16x128_f8f6f4 v[94:97], v[2:9], v[192:199], v[94:97], v189, v190 op_sel_hi:[0,0,0]
	v_mfma_scale_f32_16x16x128_f8f6f4 v[86:89], v[10:17], v[192:199], v[86:89], v189, v190 op_sel_hi:[0,0,0]
	v_mfma_scale_f32_16x16x128_f8f6f4 v[78:81], v[2:9], v[200:207], v[78:81], v189, v190 op_sel_hi:[0,0,0]
	v_mfma_scale_f32_16x16x128_f8f6f4 v[70:73], v[10:17], v[200:207], v[70:73], v189, v190 op_sel_hi:[0,0,0]
	v_mfma_scale_f32_16x16x128_f8f6f4 v[62:65], v[2:9], v[216:223], v[62:65], v189, v190 op_sel_hi:[0,0,0]
	v_mfma_scale_f32_16x16x128_f8f6f4 v[54:57], v[10:17], v[216:223], v[54:57], v189, v190 op_sel_hi:[0,0,0]
	v_mfma_scale_f32_16x16x128_f8f6f4 v[46:49], v[2:9], v[224:231], v[46:49], v189, v190 op_sel_hi:[0,0,0]
	v_mfma_scale_f32_16x16x128_f8f6f4 v[38:41], v[10:17], v[224:231], v[38:41], v189, v190 op_sel_hi:[0,0,0]
	s_setprio 0
	s_setprio 1
	v_mfma_scale_f32_16x16x128_f8f6f4 v[90:93], v[18:25], v[192:199], v[90:93], v189, v190 op_sel_hi:[0,0,0]
	v_mfma_scale_f32_16x16x128_f8f6f4 v[82:85], v[26:33], v[192:199], v[82:85], v189, v190 op_sel_hi:[0,0,0]
	v_mfma_scale_f32_16x16x128_f8f6f4 v[74:77], v[18:25], v[200:207], v[74:77], v189, v190 op_sel_hi:[0,0,0]
	v_mfma_scale_f32_16x16x128_f8f6f4 v[66:69], v[26:33], v[200:207], v[66:69], v189, v190 op_sel_hi:[0,0,0]
	v_mfma_scale_f32_16x16x128_f8f6f4 v[58:61], v[18:25], v[216:223], v[58:61], v189, v190 op_sel_hi:[0,0,0]
	v_mfma_scale_f32_16x16x128_f8f6f4 v[50:53], v[26:33], v[216:223], v[50:53], v189, v190 op_sel_hi:[0,0,0]
	v_mfma_scale_f32_16x16x128_f8f6f4 v[42:45], v[18:25], v[224:231], v[42:45], v189, v190 op_sel_hi:[0,0,0]
	v_mfma_scale_f32_16x16x128_f8f6f4 v[34:37], v[26:33], v[224:231], v[34:37], v189, v190 op_sel_hi:[0,0,0]
	s_barrier
	s_setprio 0
	s_add_i32 s70, s70, 2
	s_add_u32 s34, s34, 0x100
	s_addc_u32 s35, s35, 0
	s_add_u32 s68, s68, 0x100
	s_addc_u32 s69, s69, 0
	s_cmp_gt_u32 s70, 13

.LBB0_2427:
	s_mov_b32 s100, 0
	s_cmp_lt_i32 s78, 20
	s_cselect_b64 s[2:3], -1, 0
	s_and_b64 s[2:3], s[2:3], s[4:5]
	s_and_b64 s[0:1], s[2:3], s[0:1]
	s_andn2_b64 vcc, exec, s[0:1]
	s_cbranch_vccnz .LBB0_2448
	s_lshl_b32 s6, s58, 3
	v_readlane_b32 s0, v254, 14
	s_cmp_ge_i32 s0, s6
	v_readfirstlane_b32 s4, v0
	s_cbranch_scc1 .LBB0_2448
	v_lshrrev_b32_e32 v1, 5, v0
	v_and_b32_e32 v2, 4, v1
	v_lshrrev_b32_e32 v1, 1, v0
	v_bfe_u32 v3, v0, 2, 2
	v_and_b32_e32 v1, 24, v1
	v_bfe_u32 v4, v0, 3, 25
	s_add_u32 s42, s86, 0x2dc00000
	v_or3_b32 v2, v2, v3, v1
	v_lshlrev_b32_e32 v3, 4, v0
	v_or_b32_e32 v4, 64, v4
	s_movk_i32 s0, 0x60
	s_waitcnt lgkmcnt(0)
	v_and_b32_e32 v6, 32, v0
	s_addc_u32 s43, s87, 0
	v_and_or_b32 v5, v4, s0, v2
	v_bitop3_b32 v10, v3, v6, 48 bitop3:0x6c
	v_and_b32_e32 v11, 64, v0
	s_add_u32 s8, s86, 0x16800000
	v_mul_u32_u24_e32 v5, 0x1c00, v5
	v_or_b32_e32 v3, v10, v11
	v_readlane_b32 s7, v254, 14
	s_addc_u32 s9, s87, 0
	s_waitcnt vmcnt(0)
	v_or_b32_e32 v160, v5, v3
	v_bfe_u32 v5, v0, 2, 4
	s_movk_i32 s0, 0x70
	s_ashr_i32 s45, s7, 31
	v_and_or_b32 v4, v4, s0, v5
	s_lshr_b32 s0, s45, 29
	s_add_i32 s0, s7, s0
	s_lshr_b32 s18, s4, 6
	s_ashr_i32 s1, s0, 3
	s_and_b32 s0, s0, -8
	s_lshr_b32 s5, s4, 8
	s_lshl_b32 s44, s18, 10
	s_sub_i32 s0, s7, s0
	s_add_i32 s46, s58, 1
	s_cmp_lt_i32 s0, 0
	s_cselect_b32 s7, s46, s58
	s_mul_i32 s0, s7, s0
	s_add_i32 s0, s0, s1
	s_ashr_i32 s1, s0, 31
	s_lshr_b32 s1, s1, 26
	s_add_i32 s1, s0, s1
	s_ashr_i32 s7, s1, 6
	s_lshl_b32 s7, s7, 3
	v_mul_u32_u24_e32 v12, 0x1c00, v4
	v_lshrrev_b32_e32 v4, 3, v0
	s_sub_i32 s10, s58, s7
	v_and_or_b32 v2, v4, 32, v2
	s_min_i32 s10, s10, 8
	v_mul_u32_u24_e32 v2, 0x1c00, v2
	s_abs_i32 s11, s10
	v_or_b32_e32 v164, v2, v3
	v_cvt_f32_u32_e32 v2, s11
	s_sub_i32 s13, 0, s11
	s_andn2_b32 s1, s1, 63
	s_sub_i32 s0, s0, s1
	v_rcp_iflag_f32_e32 v2, v2
	s_abs_i32 s12, s0
	s_xor_b32 s1, s0, s10
	s_ashr_i32 s1, s1, 31
	v_mul_f32_e32 v2, 0x4f7ffffe, v2
	v_cvt_u32_f32_e32 v2, v2
	v_and_or_b32 v4, v4, 48, v5
	v_mul_u32_u24_e32 v13, 0x1c00, v4
	v_or_b32_e32 v162, v12, v3
	v_readfirstlane_b32 s16, v2
	s_mul_i32 s13, s13, s16
	s_mul_hi_u32 s13, s16, s13
	s_add_i32 s16, s16, s13
	s_mul_hi_u32 s13, s12, s16
	s_mul_i32 s16, s13, s11
	s_sub_i32 s12, s12, s16
	s_add_i32 s16, s13, 1
	s_sub_i32 s17, s12, s11
	s_cmp_ge_u32 s12, s11
	s_cselect_b32 s13, s16, s13
	s_cselect_b32 s12, s17, s12
	s_add_i32 s16, s13, 1
	s_cmp_ge_u32 s12, s11
	s_cselect_b32 s11, s16, s13
	s_xor_b32 s11, s11, s1
	s_sub_i32 s69, s11, s1
	s_mul_i32 s1, s69, s10
	s_sub_i32 s0, s0, s1
	s_add_i32 s70, s7, s0
	s_cmp_ge_i32 s70, s33
	s_cselect_b64 s[0:1], -1, 0
	s_cmp_ge_i32 s70, s57
	v_cndmask_b32_e64 v2, 0, 1, s[0:1]
	s_cselect_b64 s[0:1], -1, 0
	s_cmp_ge_i32 s70, s52
	v_or_b32_e32 v166, v13, v3
	v_cndmask_b32_e64 v3, 0, 1, s[0:1]
	s_cselect_b64 s[0:1], -1, 0
	v_readfirstlane_b32 s7, v2
	v_readfirstlane_b32 s10, v3
	s_cmp_lg_u64 s[0:1], 0
	s_addc_u32 s7, s7, s10
	s_cmp_ge_i32 s70, s53
	s_cselect_b64 s[0:1], -1, 0
	s_cmp_ge_i32 s70, s54
	v_cndmask_b32_e64 v2, 0, 1, s[0:1]
	s_cselect_b64 s[0:1], -1, 0
	v_readfirstlane_b32 s10, v2
	s_cmp_lg_u64 s[0:1], 0
	s_addc_u32 s7, s7, s10
	s_cmp_ge_i32 s70, s55
	s_cselect_b64 s[0:1], -1, 0
	s_cmp_ge_i32 s70, s56
	v_cndmask_b32_e64 v2, 0, 1, s[0:1]
	s_cselect_b64 s[0:1], -1, 0
	v_readfirstlane_b32 s10, v2
	s_cmp_lg_u64 s[0:1], 0
	s_addc_u32 s0, s7, s10
	s_lshl_b32 s0, s0, 3
	s_add_i32 s0, s0, s69
	s_mul_hi_i32 s1, s0, 0x1c0000
	s_mul_i32 s0, s0, 0x1c0000
	s_add_u32 s0, s8, s0
	s_addc_u32 s1, s9, s1
	s_add_i32 s47, s44, 0
	s_add_i32 m0, s47, 0x10000
	s_mul_i32 s12, s70, 0x1c0000
	global_load_lds_dwordx4 v164, s[0:1]
	s_add_i32 m0, s47, 0x12000
	s_add_u32 s10, s0, 0xe0000
	global_load_lds_dwordx4 v160, s[0:1]
	s_addc_u32 s11, s1, 0
	s_add_i32 m0, s47, 0x14000
	s_mul_hi_i32 s7, s70, 0x1c0000
	global_load_lds_dwordx4 v164, s[10:11]
	s_add_i32 m0, s47, 0x16000
	s_add_u32 s38, s42, s12
	s_addc_u32 s39, s43, s7
	s_add_i32 s48, s47, 0x2000
	global_load_lds_dwordx4 v160, s[10:11]
	s_mov_b32 m0, s47
	s_add_u32 s10, s38, 0xe0000
	global_load_lds_dwordx4 v166, s[38:39]
	s_mov_b32 m0, s48
	s_addc_u32 s11, s39, 0
	s_add_i32 s49, s47, 0x4000
	global_load_lds_dwordx4 v162, s[38:39]
	s_mov_b32 m0, s49
	s_add_i32 s50, s47, 0x6000
	global_load_lds_dwordx4 v166, s[10:11]
	s_mov_b32 m0, s50
	v_mov_b32_e32 v165, 0
	global_load_lds_dwordx4 v162, s[10:11]
	v_mov_b32_e32 v161, v165
	v_mov_b32_e32 v167, v165
	v_mov_b32_e32 v163, v165
	s_cmp_eq_u32 s5, 1
	s_mov_b32 s7, 0
	s_mov_b32 s51, 0x1c0000
	v_lshl_add_u64 v[8:9], s[0:1], 0, v[164:165]
	v_lshl_add_u64 v[4:5], s[0:1], 0, v[160:161]
	s_mov_b64 s[10:11], 0xe0000
	v_lshl_add_u64 v[2:3], s[38:39], 0, v[166:167]
	s_cselect_b64 s[12:13], -1, 0
	s_cmp_lg_u32 s5, 1
	v_lshl_add_u64 v[6:7], s[38:39], 0, v[162:163]
	s_cbranch_scc1 .LBB0_2431
	s_barrier

.LBB0_2440:
	s_add_u32 s38, s38, 0xe0080
	s_addc_u32 s39, s39, 0
	v_lshl_add_u64 v[176:177], v[0:1], 0, s[26:27]
	s_mov_b32 s71, -2
	ds_read_b128 v[16:19], v191
	ds_read_b128 v[20:23], v191 offset:1024
	ds_read_b128 v[24:27], v191 offset:2048
	ds_read_b128 v[28:31], v191 offset:3072
	ds_read_b128 v[0:3], v192
	ds_read_b128 v[4:7], v192 offset:1024
	ds_read_b128 v[8:11], v192 offset:2048
	ds_read_b128 v[12:15], v192 offset:3072
	s_add_u32 s40, s38, 0xfff20080
	s_addc_u32 s41, s39, -1
	s_cmp_eq_u32 s71, 52
	s_cselect_b64 vcc, -1, 0
	s_cselect_b32 s41, s1, s41
	s_cselect_b32 s40, s0, s40
	v_cndmask_b32_e32 v179, v177, v175, vcc
	v_cndmask_b32_e32 v178, v176, v174, vcc
	v_lshl_add_u64 v[214:215], s[38:39], 0, v[168:169]
	s_add_i32 m0, s47, 0xc000
	ds_read_b128 v[180:183], v193
	ds_read_b128 v[184:187], v193 offset:1024
	ds_read_b128 v[198:201], v193 offset:2048
	ds_read_b128 v[202:205], v193 offset:3072
	ds_read_b128 v[206:209], v193 offset:4096
	ds_read_b128 v[210:213], v193 offset:5120
	ds_read_b128 v[216:219], v193 offset:6144
	ds_read_b128 v[220:223], v193 offset:7168
	global_load_lds_dwordx4 v[214:215], off
	v_lshl_add_u64 v[214:215], s[38:39], 0, v[170:171]
	s_add_i32 m0, s47, 0xe000
	s_nop 0
	global_load_lds_dwordx4 v[214:215], off
	s_cmp_lg_u32 s100, 0
	s_cbranch_scc1 .Lrx_2441_0
	s_waitcnt vmcnt(8)
.Lrx_2441_0:
	s_waitcnt vmcnt(24)
	s_waitcnt lgkmcnt(0)
	s_setprio 1
	s_barrier
	v_mfma_scale_f32_16x16x128_f8f6f4 v[156:159], v[16:23], v[180:187], 0, v194, v195 op_sel_hi:[0,0,0]
	v_mfma_scale_f32_16x16x128_f8f6f4 v[152:155], v[24:31], v[180:187], 0, v194, v195 op_sel_hi:[0,0,0]
	v_mfma_scale_f32_16x16x128_f8f6f4 v[148:151], v[16:23], v[198:205], 0, v194, v195 op_sel_hi:[0,0,0]
	v_mfma_scale_f32_16x16x128_f8f6f4 v[140:143], v[24:31], v[198:205], 0, v194, v195 op_sel_hi:[0,0,0]
	v_mfma_scale_f32_16x16x128_f8f6f4 v[132:135], v[16:23], v[206:213], 0, v194, v195 op_sel_hi:[0,0,0]
	v_mfma_scale_f32_16x16x128_f8f6f4 v[124:127], v[24:31], v[206:213], 0, v194, v195 op_sel_hi:[0,0,0]
	v_mfma_scale_f32_16x16x128_f8f6f4 v[116:119], v[16:23], v[216:223], 0, v194, v195 op_sel_hi:[0,0,0]
	v_mfma_scale_f32_16x16x128_f8f6f4 v[108:111], v[24:31], v[216:223], 0, v194, v195 op_sel_hi:[0,0,0]
	s_setprio 0
	s_setprio 1
	v_mfma_scale_f32_16x16x128_f8f6f4 v[144:147], v[0:7], v[180:187], 0, v194, v195 op_sel_hi:[0,0,0]
	v_mfma_scale_f32_16x16x128_f8f6f4 v[136:139], v[8:15], v[180:187], 0, v194, v195 op_sel_hi:[0,0,0]
	v_mfma_scale_f32_16x16x128_f8f6f4 v[128:131], v[0:7], v[198:205], 0, v194, v195 op_sel_hi:[0,0,0]
	v_mfma_scale_f32_16x16x128_f8f6f4 v[120:123], v[8:15], v[198:205], 0, v194, v195 op_sel_hi:[0,0,0]
	v_mfma_scale_f32_16x16x128_f8f6f4 v[112:115], v[0:7], v[206:213], 0, v194, v195 op_sel_hi:[0,0,0]
	v_mfma_scale_f32_16x16x128_f8f6f4 v[104:107], v[8:15], v[206:213], 0, v194, v195 op_sel_hi:[0,0,0]
	v_mfma_scale_f32_16x16x128_f8f6f4 v[100:103], v[0:7], v[216:223], 0, v194, v195 op_sel_hi:[0,0,0]
	v_mfma_scale_f32_16x16x128_f8f6f4 v[96:99], v[8:15], v[216:223], 0, v194, v195 op_sel_hi:[0,0,0]
	s_barrier
	s_setprio 0
	s_add_i32 s72, s6, s44
	v_lshl_add_u64 v[180:181], v[178:179], 0, v[164:165]
	s_mov_b32 m0, s72
	ds_read_b128 v[198:201], v193 offset:16384
	ds_read_b128 v[202:205], v193 offset:17408
	ds_read_b128 v[206:209], v193 offset:18432
	ds_read_b128 v[210:213], v193 offset:19456
	ds_read_b128 v[216:219], v193 offset:20480
	ds_read_b128 v[220:223], v193 offset:21504
	ds_read_b128 v[224:227], v193 offset:22528
	ds_read_b128 v[228:231], v193 offset:23552
	global_load_lds_dwordx4 v[180:181], off
	v_lshl_add_u64 v[182:183], v[178:179], 0, v[160:161]
	s_add_i32 m0, s72, 0x2000
	v_lshl_add_u64 v[184:185], v[178:179], 0, s[10:11]
	s_add_i32 s72, s62, s44
	global_load_lds_dwordx4 v[182:183], off
	v_lshl_add_u64 v[186:187], v[184:185], 0, v[164:165]
	s_mov_b32 m0, s72
	v_lshl_add_u64 v[184:185], v[184:185], 0, v[160:161]
	global_load_lds_dwordx4 v[186:187], off
	s_add_i32 m0, s72, 0x2000
	v_lshl_add_u64 v[186:187], s[40:41], 0, v[162:163]
	global_load_lds_dwordx4 v[184:185], off
	v_lshl_add_u64 v[184:185], s[40:41], 0, v[166:167]
	s_mov_b32 m0, s47
	s_nop 0
	global_load_lds_dwordx4 v[184:185], off
	s_mov_b32 m0, s48
	s_nop 0
	global_load_lds_dwordx4 v[186:187], off
	s_cmp_lg_u32 s100, 0
	s_cbranch_scc1 .Lrx_2441_1
	s_waitcnt vmcnt(8)
.Lrx_2441_1:
	s_waitcnt vmcnt(24)
	s_mov_b32 s100, 1
	s_waitcnt lgkmcnt(0)
	s_setprio 1
	s_barrier
	v_mfma_scale_f32_16x16x128_f8f6f4 v[92:95], v[16:23], v[198:205], 0, v194, v195 op_sel_hi:[0,0,0]
	v_mfma_scale_f32_16x16x128_f8f6f4 v[88:91], v[24:31], v[198:205], 0, v194, v195 op_sel_hi:[0,0,0]
	v_mfma_scale_f32_16x16x128_f8f6f4 v[84:87], v[16:23], v[206:213], 0, v194, v195 op_sel_hi:[0,0,0]
	v_mfma_scale_f32_16x16x128_f8f6f4 v[76:79], v[24:31], v[206:213], 0, v194, v195 op_sel_hi:[0,0,0]
	v_mfma_scale_f32_16x16x128_f8f6f4 v[68:71], v[16:23], v[216:223], 0, v194, v195 op_sel_hi:[0,0,0]
	v_mfma_scale_f32_16x16x128_f8f6f4 v[60:63], v[24:31], v[216:223], 0, v194, v195 op_sel_hi:[0,0,0]
	v_mfma_scale_f32_16x16x128_f8f6f4 v[52:55], v[16:23], v[224:231], 0, v194, v195 op_sel_hi:[0,0,0]
	v_mfma_scale_f32_16x16x128_f8f6f4 v[44:47], v[24:31], v[224:231], 0, v194, v195 op_sel_hi:[0,0,0]
	s_setprio 0
	s_setprio 1
	v_mfma_scale_f32_16x16x128_f8f6f4 v[80:83], v[0:7], v[198:205], 0, v194, v195 op_sel_hi:[0,0,0]
	v_mfma_scale_f32_16x16x128_f8f6f4 v[72:75], v[8:15], v[198:205], 0, v194, v195 op_sel_hi:[0,0,0]
	v_mfma_scale_f32_16x16x128_f8f6f4 v[64:67], v[0:7], v[206:213], 0, v194, v195 op_sel_hi:[0,0,0]
	v_mfma_scale_f32_16x16x128_f8f6f4 v[56:59], v[8:15], v[206:213], 0, v194, v195 op_sel_hi:[0,0,0]
	v_mfma_scale_f32_16x16x128_f8f6f4 v[48:51], v[0:7], v[216:223], 0, v194, v195 op_sel_hi:[0,0,0]
	v_mfma_scale_f32_16x16x128_f8f6f4 v[40:43], v[8:15], v[216:223], 0, v194, v195 op_sel_hi:[0,0,0]
	v_mfma_scale_f32_16x16x128_f8f6f4 v[36:39], v[0:7], v[224:231], 0, v194, v195 op_sel_hi:[0,0,0]
	v_mfma_scale_f32_16x16x128_f8f6f4 v[32:35], v[8:15], v[224:231], 0, v194, v195 op_sel_hi:[0,0,0]
	s_barrier
	s_setprio 0
	s_add_i32 s72, 0, 0x18000
	s_add_i32 s73, 0, 0x1c000
	v_add_u32_e32 v12, s72, v189
	v_add_u32_e32 v28, s73, v189
	ds_read_b128 v[0:3], v12
	ds_read_b128 v[4:7], v12 offset:1024
	ds_read_b128 v[8:11], v12 offset:2048
	ds_read_b128 v[12:15], v12 offset:3072
	ds_read_b128 v[16:19], v28
	ds_read_b128 v[20:23], v28 offset:1024
	ds_read_b128 v[24:27], v28 offset:2048
	ds_read_b128 v[28:31], v28 offset:3072
	s_add_u32 s40, s40, 0xe0000
	s_addc_u32 s41, s41, 0
	s_mov_b32 m0, s49
	v_lshl_add_u64 v[214:215], s[40:41], 0, v[166:167]
	ds_read_b128 v[198:201], v193 offset:32768
	ds_read_b128 v[202:205], v193 offset:33792
	ds_read_b128 v[206:209], v193 offset:34816
	ds_read_b128 v[210:213], v193 offset:35840
	ds_read_b128 v[216:219], v193 offset:36864
	ds_read_b128 v[220:223], v193 offset:37888
	ds_read_b128 v[224:227], v193 offset:38912
	ds_read_b128 v[228:231], v193 offset:39936
	global_load_lds_dwordx4 v[214:215], off
	v_lshl_add_u64 v[214:215], s[40:41], 0, v[162:163]
	s_mov_b32 m0, s50
	s_nop 0
	global_load_lds_dwordx4 v[214:215], off
	s_waitcnt vmcnt(8)
	s_waitcnt lgkmcnt(0)
	s_setprio 1
	s_barrier
	v_mfma_scale_f32_16x16x128_f8f6f4 v[156:159], v[0:7], v[198:205], v[156:159], v194, v195 op_sel_hi:[0,0,0]
	v_mfma_scale_f32_16x16x128_f8f6f4 v[152:155], v[8:15], v[198:205], v[152:155], v194, v195 op_sel_hi:[0,0,0]
	v_mfma_scale_f32_16x16x128_f8f6f4 v[148:151], v[0:7], v[206:213], v[148:151], v194, v195 op_sel_hi:[0,0,0]
	v_mfma_scale_f32_16x16x128_f8f6f4 v[140:143], v[8:15], v[206:213], v[140:143], v194, v195 op_sel_hi:[0,0,0]
	v_mfma_scale_f32_16x16x128_f8f6f4 v[132:135], v[0:7], v[216:223], v[132:135], v194, v195 op_sel_hi:[0,0,0]
	v_mfma_scale_f32_16x16x128_f8f6f4 v[124:127], v[8:15], v[216:223], v[124:127], v194, v195 op_sel_hi:[0,0,0]
	v_mfma_scale_f32_16x16x128_f8f6f4 v[116:119], v[0:7], v[224:231], v[116:119], v194, v195 op_sel_hi:[0,0,0]
	v_mfma_scale_f32_16x16x128_f8f6f4 v[108:111], v[8:15], v[224:231], v[108:111], v194, v195 op_sel_hi:[0,0,0]
	s_setprio 0
	s_setprio 1
	v_mfma_scale_f32_16x16x128_f8f6f4 v[144:147], v[16:23], v[198:205], v[144:147], v194, v195 op_sel_hi:[0,0,0]
	v_mfma_scale_f32_16x16x128_f8f6f4 v[136:139], v[24:31], v[198:205], v[136:139], v194, v195 op_sel_hi:[0,0,0]
	v_mfma_scale_f32_16x16x128_f8f6f4 v[128:131], v[16:23], v[206:213], v[128:131], v194, v195 op_sel_hi:[0,0,0]
	v_mfma_scale_f32_16x16x128_f8f6f4 v[120:123], v[24:31], v[206:213], v[120:123], v194, v195 op_sel_hi:[0,0,0]
	v_mfma_scale_f32_16x16x128_f8f6f4 v[112:115], v[16:23], v[216:223], v[112:115], v194, v195 op_sel_hi:[0,0,0]
	v_mfma_scale_f32_16x16x128_f8f6f4 v[104:107], v[24:31], v[216:223], v[104:107], v194, v195 op_sel_hi:[0,0,0]
	v_mfma_scale_f32_16x16x128_f8f6f4 v[100:103], v[16:23], v[224:231], v[100:103], v194, v195 op_sel_hi:[0,0,0]
	v_mfma_scale_f32_16x16x128_f8f6f4 v[96:99], v[24:31], v[224:231], v[96:99], v194, v195 op_sel_hi:[0,0,0]
	s_barrier
	s_setprio 0
	s_add_i32 s40, s72, s44
	v_lshl_add_u64 v[180:181], v[180:181], 0, s[18:19]
	s_mov_b32 m0, s40
	ds_read_b128 v[198:201], v193 offset:49152
	ds_read_b128 v[202:205], v193 offset:50176
	ds_read_b128 v[206:209], v193 offset:51200
	ds_read_b128 v[210:213], v193 offset:52224
	ds_read_b128 v[216:219], v193 offset:53248
	ds_read_b128 v[220:223], v193 offset:54272
	ds_read_b128 v[224:227], v193 offset:55296
	ds_read_b128 v[228:231], v193 offset:56320
	global_load_lds_dwordx4 v[180:181], off
	v_lshl_add_u64 v[180:181], v[182:183], 0, s[18:19]
	s_add_i32 m0, s40, 0x2000
	v_lshl_add_u64 v[178:179], v[178:179], 0, s[22:23]
	s_add_i32 s40, s73, s44
	global_load_lds_dwordx4 v[180:181], off
	v_lshl_add_u64 v[180:181], v[178:179], 0, v[164:165]
	s_mov_b32 m0, s40
	v_lshl_add_u64 v[178:179], v[178:179], 0, v[160:161]
	global_load_lds_dwordx4 v[180:181], off
	s_add_i32 m0, s40, 0x2000
	s_nop 0
	global_load_lds_dwordx4 v[178:179], off
	v_lshl_add_u64 v[178:179], v[184:185], 0, s[18:19]
	s_mov_b32 m0, s59
	s_nop 0
	global_load_lds_dwordx4 v[178:179], off
	v_lshl_add_u64 v[178:179], v[186:187], 0, s[18:19]
	s_mov_b32 m0, s60
	s_nop 0
	global_load_lds_dwordx4 v[178:179], off
	s_waitcnt vmcnt(8)
	s_waitcnt lgkmcnt(0)
	s_setprio 1
	s_barrier
	v_mfma_scale_f32_16x16x128_f8f6f4 v[92:95], v[0:7], v[198:205], v[92:95], v194, v195 op_sel_hi:[0,0,0]
	v_mfma_scale_f32_16x16x128_f8f6f4 v[88:91], v[8:15], v[198:205], v[88:91], v194, v195 op_sel_hi:[0,0,0]
	v_mfma_scale_f32_16x16x128_f8f6f4 v[84:87], v[0:7], v[206:213], v[84:87], v194, v195 op_sel_hi:[0,0,0]
	v_mfma_scale_f32_16x16x128_f8f6f4 v[76:79], v[8:15], v[206:213], v[76:79], v194, v195 op_sel_hi:[0,0,0]
	v_mfma_scale_f32_16x16x128_f8f6f4 v[68:71], v[0:7], v[216:223], v[68:71], v194, v195 op_sel_hi:[0,0,0]
	v_mfma_scale_f32_16x16x128_f8f6f4 v[60:63], v[8:15], v[216:223], v[60:63], v194, v195 op_sel_hi:[0,0,0]
	v_mfma_scale_f32_16x16x128_f8f6f4 v[52:55], v[0:7], v[224:231], v[52:55], v194, v195 op_sel_hi:[0,0,0]
	v_mfma_scale_f32_16x16x128_f8f6f4 v[44:47], v[8:15], v[224:231], v[44:47], v194, v195 op_sel_hi:[0,0,0]
	s_setprio 0
	s_setprio 1
	v_mfma_scale_f32_16x16x128_f8f6f4 v[80:83], v[16:23], v[198:205], v[80:83], v194, v195 op_sel_hi:[0,0,0]
	v_mfma_scale_f32_16x16x128_f8f6f4 v[72:75], v[24:31], v[198:205], v[72:75], v194, v195 op_sel_hi:[0,0,0]
	v_mfma_scale_f32_16x16x128_f8f6f4 v[64:67], v[16:23], v[206:213], v[64:67], v194, v195 op_sel_hi:[0,0,0]
	v_mfma_scale_f32_16x16x128_f8f6f4 v[56:59], v[24:31], v[206:213], v[56:59], v194, v195 op_sel_hi:[0,0,0]
	v_mfma_scale_f32_16x16x128_f8f6f4 v[48:51], v[16:23], v[216:223], v[48:51], v194, v195 op_sel_hi:[0,0,0]
	v_mfma_scale_f32_16x16x128_f8f6f4 v[40:43], v[24:31], v[216:223], v[40:43], v194, v195 op_sel_hi:[0,0,0]
	v_mfma_scale_f32_16x16x128_f8f6f4 v[36:39], v[16:23], v[224:231], v[36:39], v194, v195 op_sel_hi:[0,0,0]
	v_mfma_scale_f32_16x16x128_f8f6f4 v[32:35], v[24:31], v[224:231], v[32:35], v194, v195 op_sel_hi:[0,0,0]
	s_barrier
	s_setprio 0
	s_add_i32 s71, s71, 2
	s_add_u32 s38, s38, 0x100
	s_addc_u32 s39, s39, 0
	s_cmp_gt_u32 s71, 53
	v_lshl_add_u64 v[176:177], v[176:177], 0, s[26:27]
